# attention pair-mask LUT + MFMA row sums; indexer histogram scan rewritten (4 queries per wave at once, conflict-free LDS order, DPP row scans)
# speedup vs baseline: 1.0266x; 1.0266x over previous
; #define LAS __attribute__((address_space(3)))
; template <bool L2> __device__ __forceinline__ void idx_scan(LAS unsigned* row, bool positive, unsigned need, int lane, unsigned& bin_out, unsigned& need_out) {
;     asm volatile("" : "+v"(lane));
;     unsigned c[16], sum = 0;
; #pragma unroll
;     for (int i = 0; i < 16; ++i) { const int p = 16 * lane + i; const int bin = L2 ? (positive ? 1023 - p : p) : (p < 512 ? 511 - p : p); c[i] = row[bin]; row[bin] = 0u; sum += c[i]; }
;     unsigned incl = sum;
; #pragma unroll
;     for (int o = 1; o < 64; o <<= 1) { const unsigned v = __shfl_up(incl, o); if (lane >= o) incl += v; }
;     const unsigned long long m = __ballot(incl >= need);
;     const int Ls = m ? (int)__builtin_ctzll(m) : 63;
;     unsigned cum = incl - sum, fb = 0u, fn = 1u; bool found = false;
; #pragma unroll
;     for (int i = 0; i < 16; ++i) { const int p = 16 * lane + i; const unsigned bin = (unsigned)(L2 ? (positive ? 1023 - p : p) : (p < 512 ? 511 - p : p));
;         if (!found && cum + c[i] >= need) { found = true; fb = bin; fn = need - cum; } cum += c[i]; }
;     bin_out = (unsigned)__shfl((int)fb, Ls); need_out = (unsigned)__shfl((int)fn, Ls);
; }
.LBB0_995:
	v_cmp_eq_u32_e32 vcc, 0, v212
	s_mov_b32 s18, 4
	s_mul_i32 s44, s38, 0x4010
	v_readlane_b32 s45, v252, 33
	s_waitcnt lgkmcnt(0)
	s_barrier
	s_mov_b64 s[64:65], exec
	s_mov_b64 exec, -1
	s_movk_i32 s46, 0x1004
	s_movk_i32 s47, 0x100
	v_and_b32_e32 v1, 15, v212
	v_lshrrev_b32_e32 v2, 4, v212
	v_mov_b32_e32 v5, s44
	v_mad_u32_u24 v4, v2, s46, v5
	v_cmp_gt_u32_e64 s[58:59], 8, v1
	v_lshlrev_b32_e32 v6, 8, v1
	v_sub_u32_e32 v7, 0x73c, v6
	s_nop 0
	v_cndmask_b32_e64 v6, v6, v7, s[58:59]
	v_add_u32_e32 v6, v4, v6
	v_mov_b32_e32 v7, 4
	v_cndmask_b32_e64 v7, v7, -4, s[58:59]
	v_xor_b32_e32 v8, 0, v1
	v_mad_i32_i24 v9, v8, v7, v6
	ds_read2_b32 v[146:147], v9 offset1:16
	ds_read2_b32 v[148:149], v9 offset0:32 offset1:48
	v_xor_b32_e32 v8, 1, v1
	v_mad_i32_i24 v10, v8, v7, v6
	ds_read2_b32 v[150:151], v10 offset1:16
	ds_read2_b32 v[152:153], v10 offset0:32 offset1:48
	v_xor_b32_e32 v8, 2, v1
	v_mad_i32_i24 v11, v8, v7, v6
	ds_read2_b32 v[154:155], v11 offset1:16
	ds_read2_b32 v[156:157], v11 offset0:32 offset1:48
	v_xor_b32_e32 v8, 3, v1
	v_mad_i32_i24 v12, v8, v7, v6
	ds_read2_b32 v[158:159], v12 offset1:16
	ds_read2_b32 v[160:161], v12 offset0:32 offset1:48
	v_xor_b32_e32 v8, 4, v1
	v_mad_i32_i24 v13, v8, v7, v6
	ds_read2_b32 v[162:163], v13 offset1:16
	ds_read2_b32 v[164:165], v13 offset0:32 offset1:48
	v_xor_b32_e32 v8, 5, v1
	v_mad_i32_i24 v14, v8, v7, v6
	ds_read2_b32 v[166:167], v14 offset1:16
	ds_read2_b32 v[168:169], v14 offset0:32 offset1:48
	v_xor_b32_e32 v8, 6, v1
	v_mad_i32_i24 v15, v8, v7, v6
	ds_read2_b32 v[170:171], v15 offset1:16
	ds_read2_b32 v[172:173], v15 offset0:32 offset1:48
	v_xor_b32_e32 v8, 7, v1
	v_mad_i32_i24 v16, v8, v7, v6
	ds_read2_b32 v[174:175], v16 offset1:16
	ds_read2_b32 v[176:177], v16 offset0:32 offset1:48
	v_xor_b32_e32 v8, 8, v1
	v_mad_i32_i24 v17, v8, v7, v6
	ds_read2_b32 v[178:179], v17 offset1:16
	ds_read2_b32 v[180:181], v17 offset0:32 offset1:48
	v_xor_b32_e32 v8, 9, v1
	v_mad_i32_i24 v18, v8, v7, v6
	ds_read2_b32 v[182:183], v18 offset1:16
	ds_read2_b32 v[184:185], v18 offset0:32 offset1:48
	v_xor_b32_e32 v8, 10, v1
	v_mad_i32_i24 v19, v8, v7, v6
	ds_read2_b32 v[186:187], v19 offset1:16
	ds_read2_b32 v[188:189], v19 offset0:32 offset1:48
	v_xor_b32_e32 v8, 11, v1
	v_mad_i32_i24 v20, v8, v7, v6
	ds_read2_b32 v[190:191], v20 offset1:16
	ds_read2_b32 v[192:193], v20 offset0:32 offset1:48
	v_xor_b32_e32 v8, 12, v1
	v_mad_i32_i24 v21, v8, v7, v6
	ds_read2_b32 v[40:41], v21 offset1:16
	ds_read2_b32 v[42:43], v21 offset0:32 offset1:48
	v_xor_b32_e32 v8, 13, v1
	v_mad_i32_i24 v22, v8, v7, v6
	ds_read2_b32 v[44:45], v22 offset1:16
	ds_read2_b32 v[46:47], v22 offset0:32 offset1:48
	v_xor_b32_e32 v8, 14, v1
	v_mad_i32_i24 v23, v8, v7, v6
	ds_read2_b32 v[48:49], v23 offset1:16
	ds_read2_b32 v[50:51], v23 offset0:32 offset1:48
	v_xor_b32_e32 v8, 15, v1
	v_mad_i32_i24 v24, v8, v7, v6
	ds_read2_b32 v[52:53], v24 offset1:16
	ds_read2_b32 v[54:55], v24 offset0:32 offset1:48
	s_waitcnt lgkmcnt(0)
	v_add3_u32 v26, v146, v147, v148
	v_add3_u32 v26, v26, v149, v150
	v_add3_u32 v26, v26, v151, v152
	v_add3_u32 v26, v26, v153, v154
	v_add3_u32 v26, v26, v155, v156
	v_add3_u32 v26, v26, v157, v158
	v_add3_u32 v26, v26, v159, v160
	v_add3_u32 v26, v26, v161, v162
	v_add3_u32 v26, v26, v163, v164
	v_add3_u32 v26, v26, v165, v166
	v_add3_u32 v26, v26, v167, v168
	v_add3_u32 v26, v26, v169, v170
	v_add3_u32 v26, v26, v171, v172
	v_add3_u32 v26, v26, v173, v174
	v_add3_u32 v26, v26, v175, v176
	v_add3_u32 v26, v26, v177, v178
	v_add3_u32 v26, v26, v179, v180
	v_add3_u32 v26, v26, v181, v182
	v_add3_u32 v26, v26, v183, v184
	v_add3_u32 v26, v26, v185, v186
	v_add3_u32 v26, v26, v187, v188
	v_add3_u32 v26, v26, v189, v190
	v_add3_u32 v26, v26, v191, v192
	v_add3_u32 v26, v26, v193, v40
	v_add3_u32 v26, v26, v41, v42
	v_add3_u32 v26, v26, v43, v44
	v_add3_u32 v26, v26, v45, v46
	v_add3_u32 v26, v26, v47, v48
	v_add3_u32 v26, v26, v49, v50
	v_add3_u32 v26, v26, v51, v52
	v_add3_u32 v26, v26, v53, v54
	v_add_u32_e32 v26, v26, v55
	v_mov_b32_e32 v27, v26
	s_nop 1
	v_add_u32_dpp v27, v27, v27 row_shr:1 row_mask:0xf bank_mask:0xf bound_ctrl:0
	s_nop 1
	v_add_u32_dpp v27, v27, v27 row_shr:2 row_mask:0xf bank_mask:0xf bound_ctrl:0
	s_nop 1
	v_add_u32_dpp v27, v27, v27 row_shr:4 row_mask:0xf bank_mask:0xf bound_ctrl:0
	s_nop 1
	v_add_u32_dpp v27, v27, v27 row_shr:8 row_mask:0xf bank_mask:0xf bound_ctrl:0
	v_sub_u32_e32 v28, v27, v26
	v_cmp_gt_u32_e64 s[60:61], s47, v28
	v_cmp_le_u32_e64 s[62:63], s47, v27
	s_and_b64 s[60:61], s[60:61], s[62:63]
	v_or_b32_e32 v29, 16, v1
	v_cndmask_b32_e64 v29, 0, v29, s[60:61]
	v_cndmask_b32_e64 v30, 0, v28, s[60:61]
	s_nop 1
	v_or_b32_dpp v29, v29, v29 quad_perm:[1,0,3,2] row_mask:0xf bank_mask:0xf
	v_or_b32_dpp v30, v30, v30 quad_perm:[1,0,3,2] row_mask:0xf bank_mask:0xf
	s_nop 1
	v_or_b32_dpp v29, v29, v29 quad_perm:[2,3,0,1] row_mask:0xf bank_mask:0xf
	v_or_b32_dpp v30, v30, v30 quad_perm:[2,3,0,1] row_mask:0xf bank_mask:0xf
	s_nop 1
	v_or_b32_dpp v29, v29, v29 row_half_mirror row_mask:0xf bank_mask:0xf
	v_or_b32_dpp v30, v30, v30 row_half_mirror row_mask:0xf bank_mask:0xf
	s_nop 1
	v_or_b32_dpp v29, v29, v29 row_mirror row_mask:0xf bank_mask:0xf
	v_or_b32_dpp v30, v30, v30 row_mirror row_mask:0xf bank_mask:0xf
	s_nop 1
	v_and_b32_e32 v31, 15, v29
	v_cmp_gt_u32_e64 s[58:59], 8, v31
	v_lshlrev_b32_e32 v32, 6, v31
	v_lshl_add_u32 v32, v1, 2, v32
	v_sub_u32_e32 v33, 0x1fc, v32
	s_nop 0
	v_cndmask_b32_e64 v33, v32, v33, s[58:59]
	v_lshl_add_u32 v33, v33, 2, v4
	ds_read2_b32 v[34:35], v33 offset1:1
	ds_read2_b32 v[36:37], v33 offset0:2 offset1:3
	s_waitcnt lgkmcnt(0)
; __device__ __forceinline__ unsigned ix_mono(unsigned raw) { return (raw & 0x80000000u) ? ~raw : (raw | 0x80000000u); }
; __device__ __forceinline__ float ix_h2f(unsigned h) { return (float)__builtin_bit_cast(_Float16, (unsigned short)h); }
; template <bool L2> __device__ __forceinline__ void idx_scan(LAS unsigned* row, bool positive, unsigned need, int lane, unsigned& bin_out, unsigned& need_out) {
;     ...
;     for (int i = 0; i < 16; ++i) { const int p = 16 * lane + i; const int bin = L2 ? (positive ? 1023 - p : p) : (p < 512 ? 511 - p : p); c[i] = row[bin]; row[bin] = 0u; sum += c[i]; }
;     unsigned incl = sum;
; #pragma unroll
;     for (int o = 1; o < 64; o <<= 1) { const unsigned v = __shfl_up(incl, o); if (lane >= o) incl += v; }
;     const unsigned long long m = __ballot(incl >= need);
;     const int Ls = m ? (int)__builtin_ctzll(m) : 63;
;     unsigned cum = incl - sum, fb = 0u, fn = 1u; bool found = false;
; #pragma unroll
;     for (int i = 0; i < 16; ++i) { const int p = 16 * lane + i; const unsigned bin = (unsigned)(L2 ? (positive ? 1023 - p : p) : (p < 512 ? 511 - p : p));
;         if (!found && cum + c[i] >= need) { found = true; fb = bin; fn = need - cum; } cum += c[i]; }
;     bin_out = (unsigned)__shfl((int)fb, Ls); need_out = (unsigned)__shfl((int)fn, Ls);
; }
; __device__ __forceinline__ void idx_unit(Frame& F, const bf16* QI, const bf16* KI, const float* WI, unsigned* MASK, int b, int j) {
;     ...
;         for (int qq = wave * 4; qq < wave * 4 + 4; ++qq) { unsigned bn, nd; idx_scan<false>(hist + qq * IX_HS, true, 256u, lane, bn, nd);
;             if (lane == 0) {
;                 float tsv, tiv;
;                 if (bn < 512u) { tiv = ix_h2f(bn << 6); tsv = ix_h2f((bn + 1u) << 6); }
;                 else { const unsigned mb = bn - 512u; const float mlo = ix_h2f(mb << 6), mhi = ix_h2f((mb + 1u) << 6);
;                     tsv = (mlo == 0.f) ? 0.f : __uint_as_float(__float_as_uint(-mlo) - 1u); tiv = __uint_as_float(__float_as_uint(-mhi) - 1u); }
;                 st[qq] = bn; st[32 + qq] = nd; st[64 + qq] = __float_as_uint(tsv); st[96 + qq] = __float_as_uint(tiv); st[128 + qq] = ix_mono(__float_as_uint(tiv)); st[160 + qq] = 0u; } }
	v_cndmask_b32_e64 v56, v34, v37, s[58:59]
	v_cndmask_b32_e64 v57, v35, v36, s[58:59]
	v_cndmask_b32_e64 v58, v36, v35, s[58:59]
	v_cndmask_b32_e64 v59, v37, v34, s[58:59]
	v_add3_u32 v60, v56, v57, v58
	v_add_u32_e32 v60, v60, v59
	v_mov_b32_e32 v61, v60
	s_nop 1
	v_add_u32_dpp v61, v61, v61 row_shr:1 row_mask:0xf bank_mask:0xf bound_ctrl:0
	s_nop 1
	v_add_u32_dpp v61, v61, v61 row_shr:2 row_mask:0xf bank_mask:0xf bound_ctrl:0
	s_nop 1
	v_add_u32_dpp v61, v61, v61 row_shr:4 row_mask:0xf bank_mask:0xf bound_ctrl:0
	s_nop 1
	v_add_u32_dpp v61, v61, v61 row_shr:8 row_mask:0xf bank_mask:0xf bound_ctrl:0
	v_sub_u32_e32 v62, v61, v60
	v_add_u32_e32 v62, v62, v30
	v_add_u32_e32 v63, v62, v56
	v_add_u32_e32 v64, v63, v57
	v_add_u32_e32 v65, v64, v58
	v_add_u32_e32 v66, v65, v59
	v_cmp_gt_u32_e64 s[60:61], s47, v62
	v_cmp_le_u32_e64 s[62:63], s47, v66
	s_and_b64 s[60:61], s[60:61], s[62:63]
	v_cmp_le_u32_e64 s[62:63], s47, v65
	v_mov_b32_e32 v67, 3
	s_nop 1
	v_cndmask_b32_e64 v67, v67, 2, s[62:63]
	v_cndmask_b32_e64 v68, v65, v64, s[62:63]
	v_cmp_le_u32_e64 s[62:63], s47, v64
	s_nop 1
	v_cndmask_b32_e64 v67, v67, 1, s[62:63]
	v_cndmask_b32_e64 v68, v68, v63, s[62:63]
	v_cmp_le_u32_e64 s[62:63], s47, v63
	s_nop 1
	v_cndmask_b32_e64 v67, v67, 0, s[62:63]
	v_cndmask_b32_e64 v68, v68, v62, s[62:63]
	v_add_u32_e32 v69, v32, v67
	v_sub_u32_e32 v70, 0x1ff, v69
	s_movk_i32 s53, 0x200
	v_cmp_gt_u32_e64 s[62:63], s53, v69
	s_nop 1
	v_cndmask_b32_e64 v69, v69, v70, s[62:63]
	v_sub_u32_e32 v70, 0x100, v68
	v_bfe_u32 v71, v29, 4, 1
	v_cmp_eq_u32_e64 s[62:63], 0, v71
	v_cmp_eq_u32_e64 s[58:59], 0, v1
	s_and_b64 s[62:63], s[62:63], s[58:59]
	v_cndmask_b32_e64 v69, v69, 0, s[62:63]
	v_cndmask_b32_e64 v70, v70, 1, s[62:63]
	s_or_b64 s[60:61], s[60:61], s[62:63]
	s_mov_b64 exec, s[60:61]
	v_lshlrev_b16_e32 v72, 6, v69
	v_add_u16_e32 v74, 64, v72
	v_add_u16_e32 v75, 0x8040, v72
	v_cvt_f32_f16_e32 v73, v72
	v_cvt_f32_f16_e32 v74, v74
	v_cvt_f32_f16_e64 v75, -v75
	v_add_u32_e32 v76, -1, v73
	v_add_u32_e32 v75, -1, v75
	s_mov_b32 s55, 0x8000
	v_cmp_neq_f16_e64 s[62:63], s55, v72
	s_nop 1
	v_cndmask_b32_e64 v76, 0, v76, s[62:63]
	s_movk_i32 s57, 0x1ff
	v_cmp_lt_u32_e64 s[62:63], s57, v69
	s_nop 1
	v_cndmask_b32_e64 v74, v74, v76, s[62:63]
	v_cndmask_b32_e64 v73, v73, v75, s[62:63]
	v_not_b32_e32 v77, v73
	v_cmp_gt_i32_e64 s[62:63], 0, v73
	s_nop 1
	v_cndmask_b32_e64 v77, -|v73|, v77, s[62:63]
	v_lshl_add_u32 v78, v2, 2, s45
	v_add_u32_e32 v78, 0x20080, v78
	ds_write_b32 v78, v69
	ds_write_b32 v78, v70 offset:128
	ds_write_b32 v78, v74 offset:256
	ds_write_b32 v78, v73 offset:384
	ds_write_b32 v78, v77 offset:512
	ds_write_b32 v78, v3 offset:640
	s_mov_b64 exec, -1
	v_lshl_add_u32 v79, v212, 2, s44
	ds_write2st64_b32 v79, v3, v3 offset0:0 offset1:1
	ds_write2st64_b32 v79, v3, v3 offset0:2 offset1:3
	ds_write2st64_b32 v79, v3, v3 offset0:4 offset1:5
	ds_write2st64_b32 v79, v3, v3 offset0:6 offset1:7
	ds_write2st64_b32 v79, v3, v3 offset0:8 offset1:9
	ds_write2st64_b32 v79, v3, v3 offset0:10 offset1:11
	ds_write2st64_b32 v79, v3, v3 offset0:12 offset1:13
	ds_write2st64_b32 v79, v3, v3 offset0:14 offset1:15
	ds_write2st64_b32 v79, v3, v3 offset0:16 offset1:17
	ds_write2st64_b32 v79, v3, v3 offset0:18 offset1:19
	ds_write2st64_b32 v79, v3, v3 offset0:20 offset1:21
	ds_write2st64_b32 v79, v3, v3 offset0:22 offset1:23
	ds_write2st64_b32 v79, v3, v3 offset0:24 offset1:25
	ds_write2st64_b32 v79, v3, v3 offset0:26 offset1:27
	ds_write2st64_b32 v79, v3, v3 offset0:28 offset1:29
	ds_write2st64_b32 v79, v3, v3 offset0:30 offset1:31
	ds_write2st64_b32 v79, v3, v3 offset0:32 offset1:33
	ds_write2st64_b32 v79, v3, v3 offset0:34 offset1:35
	ds_write2st64_b32 v79, v3, v3 offset0:36 offset1:37
	ds_write2st64_b32 v79, v3, v3 offset0:38 offset1:39
	ds_write2st64_b32 v79, v3, v3 offset0:40 offset1:41
	ds_write2st64_b32 v79, v3, v3 offset0:42 offset1:43
	ds_write2st64_b32 v79, v3, v3 offset0:44 offset1:45
	ds_write2st64_b32 v79, v3, v3 offset0:46 offset1:47
	ds_write2st64_b32 v79, v3, v3 offset0:48 offset1:49
	ds_write2st64_b32 v79, v3, v3 offset0:50 offset1:51
	ds_write2st64_b32 v79, v3, v3 offset0:52 offset1:53
	ds_write2st64_b32 v79, v3, v3 offset0:54 offset1:55
	ds_write2st64_b32 v79, v3, v3 offset0:56 offset1:57
	ds_write2st64_b32 v79, v3, v3 offset0:58 offset1:59
	ds_write2st64_b32 v79, v3, v3 offset0:60 offset1:61
	ds_write2st64_b32 v79, v3, v3 offset0:62 offset1:63
	v_cmp_gt_u32_e64 s[62:63], 4, v212
	s_nop 1
	s_mov_b64 exec, s[62:63]
	ds_write_b32 v79, v3 offset:16384
	s_mov_b64 exec, s[64:65]

;   #define DMA_K(t,slot) glds16(ksrc+(long)(t)*KVBLK*DM,(unsigned)__builtin_amdgcn_readfirstlane(kdst+(slot)))
;   #define DMA_V(t,slot) glds16(vsrc+(long)(t)*KVBLK*DM,(unsigned)__builtin_amdgcn_readfirstlane(vdst+(slot)))
;   #define WLOAD(W,t) asm volatile("global_load_dword %0, %1, off":"=v"(W):"v"(mwl+(size_t)(t)*64):"memory")
; template<int THRL> __device__ __forceinline__ void attn_unit(int b,int h,int qb,const bf16*Q,const bf16*__restrict__ K,const bf16*__restrict__ V,bf16*O,const unsigned*MASK,char*shm){
;   int tid_=threadIdx.x; asm volatile("":"+v"(tid_));
;   const int tid=tid_,lane=tid&63,r32=lane&31,hi=lane>>5; const int wid=__builtin_amdgcn_readfirstlane(tid>>6);
;   const long rowbase=(long)b*SEQ; const int q0=qb*QB;
;   const bf16*Qw=Q+(rowbase+q0+wid*QBLK)*DM+h*D;
;   const bf16*Kh=K+rowbase*DM+h*D,*Vh=V+rowbase*DM+h*D;
;   const unsigned lds0=(unsigned)(uintptr_t)shm;
;   float*wsf=(float*)(shm+LDS_WS)+wid*64;
;   const bf16*ksrc=Kh+(long)lane*DM+wid*8;
;   const bf16*vsrc=Vh+(long)(16*(wid&3)+(lane>>2))*DM+(wid>>2)*32+(lane&3)*8;
;   const unsigned kdst=lds0+LDS_K+wid*1024, vdst=lds0+LDS_V+wid*1024;
;     ...
;   const int vb0=(int)(lds0+LDS_V)+((lane>>4)&1)*32+(lane&3)*8+(4*hi+((lane&15)>>2))*64;
;   const char*Kbase=shm+LDS_K; bf16x8 kf[8];
;   const lds_cptr shm3=(lds_cptr)shm; const lds_cptr kp0=shm3+LDS_K+hi*1024+r32*16; const lds_cptr vp0=shm3+LDS_V+((lane>>4)&1)*32+(lane&3)*8+(4*hi+((lane&15)>>2))*64;
;   const int NT=(q0+QB)/KVBLK;
;   const unsigned*mwl=MASK+((size_t)(b*256+qb*8+wid)*128)*64+lane;
;   unsigned wA,wB;
;     ...
;   WLOAD(wA,0);WLOAD(wB,1);
;   DMA_K(0,0);DMA_V(0,0);DMA_K(1,SLOTB);
;   bf16x8 qr[4];
;   #pragma unroll
;   for(int d0=0;d0<4;++d0)qr[d0]=*reinterpret_cast<const bf16x8*>(&Qw[(long)r32*DM+d0*16+hi*8]);
;   float mhat=0.f,l_reg=0.f;f32x16 o[2];o[0]=f32x16{};o[1]=f32x16{};f32x16 negm=f32x16{};asm volatile("":"+v"(negm));
.LBB0_1271:
	s_ashr_i32 s4, s6, 31
	s_lshr_b32 s4, s4, 29
	s_add_i32 s4, s6, s4
	s_ashr_i32 s42, s4, 3
	v_mov_b32_e32 v58, v0
	s_and_b32 s4, s4, 0x3fffff8
	s_ashr_i32 s43, s42, 31
	v_readfirstlane_b32 s50, v58
	s_lshl_b32 s51, s56, 8
	s_sub_i32 s38, s6, s4
	s_ashr_i32 s7, s50, 6
	s_lshl_b64 s[4:5], s[42:43], 13
	s_ashr_i32 s39, s51, 31
	s_add_u32 s4, s4, s51
	s_addc_u32 s5, s5, s39
	s_lshl_b32 s39, s7, 5
	s_ashr_i32 s40, s39, 31
	s_add_u32 s44, s4, s39
	s_addc_u32 s45, s5, s40
	s_lshl_b64 s[4:5], s[44:45], 10
	s_add_u32 s40, s8, s4
	s_addc_u32 s41, s9, s5
	s_lshl_b32 s4, s38, 6
	s_ashr_i32 s5, s4, 31
	s_lshl_b64 s[38:39], s[4:5], 1
	s_add_u32 s40, s40, s38
	s_addc_u32 s41, s41, s39
	s_lshl_b64 s[4:5], s[42:43], 23
	s_add_u32 s43, s17, s4
	s_addc_u32 s47, s18, s5
	s_add_u32 s46, s43, s38
	s_addc_u32 s47, s47, s39
	s_add_u32 s4, s19, s4
	v_and_b32_e32 v1, 63, v58
	s_addc_u32 s5, s20, s5
	s_add_u32 s48, s4, s38
	v_lshlrev_b32_e32 v2, 10, v1
	s_addc_u32 s49, s5, s39
	v_lshl_add_u64 v[4:5], s[46:47], 0, v[2:3]
	s_lshl_b32 s46, s7, 3
	s_lshl_b32 s4, s7, 4
	v_bfe_u32 v2, v58, 2, 4
	s_ashr_i32 s47, s46, 31
	v_and_or_b32 v2, s4, 48, v2
	s_ashr_i32 s4, s50, 3
	v_lshl_add_u64 v[194:195], s[46:47], 1, v[4:5]
	s_and_b32 s46, s4, 0xffffffe0
	s_and_b32 s5, s50, 0x3fffffc0
	s_ashr_i32 s47, s46, 31
	s_lshl_b32 s58, s7, 10
	s_cmp_lg_u32 0, -1
	s_cselect_b32 s4, 0, 0
	s_lshl_b32 s42, s42, 8
	s_lshl_b32 s43, s56, 3
	s_add_i32 s42, s42, s43
	s_add_i32 s42, s42, s7
	v_lshlrev_b32_e32 v2, 10, v2
	v_lshlrev_b32_e32 v212, 3, v58
	s_add_i32 s58, s58, s4
	s_ashr_i32 s43, s42, 31
	v_lshl_add_u64 v[4:5], s[48:49], 0, v[2:3]
	v_and_b32_e32 v215, 24, v212
	s_add_i32 s59, s58, 0x6000
	s_add_i32 s4, s51, 0x100
	s_lshl_b64 s[42:43], s[42:43], 15
	v_lshl_add_u64 v[4:5], s[46:47], 1, v[4:5]
	v_lshlrev_b32_e32 v2, 1, v215
	s_add_u32 s42, s23, s42
	v_lshl_add_u64 v[208:209], v[4:5], 0, v[2:3]
	s_addc_u32 s43, s54, s43
	v_lshlrev_b32_e32 v2, 2, v1
	v_lshl_add_u64 v[84:85], s[42:43], 0, v[2:3]
	global_load_dword v59, v[84:85], off
	s_waitcnt vmcnt(0)
	v_lshlrev_b32_sdwa v225, s32, v59 dst_sel:DWORD dst_unused:UNUSED_PAD src0_sel:DWORD src1_sel:BYTE_0
	v_lshlrev_b32_sdwa v226, s32, v59 dst_sel:DWORD dst_unused:UNUSED_PAD src0_sel:DWORD src1_sel:BYTE_1
	v_lshlrev_b32_sdwa v248, s32, v59 dst_sel:DWORD dst_unused:UNUSED_PAD src0_sel:DWORD src1_sel:BYTE_2
	v_lshlrev_b32_sdwa v249, s32, v59 dst_sel:DWORD dst_unused:UNUSED_PAD src0_sel:DWORD src1_sel:BYTE_3
	v_lshl_add_u64 v[186:187], v[84:85], 0, s[30:31]
	global_load_dword v218, v[186:187], off
	v_and_b32_e32 v213, 31, v58
	s_mov_b32 s42, m0
	s_mov_b32 m0, s58
	s_nop 0
	global_load_lds_dwordx4 v[194:195], off
	s_mov_b32 m0, s42
	v_bfe_u32 v214, v58, 5, 1
	s_mov_b32 s42, m0
	s_mov_b32 m0, s59
	s_nop 0
	global_load_lds_dwordx4 v[208:209], off
	s_mov_b32 m0, s42
	v_lshlrev_b32_e32 v2, 10, v213
	v_lshl_add_u64 v[4:5], v[194:195], 0, s[36:37]
	s_add_i32 s42, s58, 0x2000
	s_mov_b32 s43, m0
	s_mov_b32 m0, s42
	s_nop 0
	global_load_lds_dwordx4 v[4:5], off
	s_mov_b32 m0, s43
	v_lshl_or_b32 v2, v214, 4, v2
	global_load_dwordx4 v[138:141], v2, s[40:41]
	global_load_dwordx4 v[134:137], v2, s[40:41] offset:32
	global_load_dwordx4 v[126:129], v2, s[40:41] offset:64
	global_load_dwordx4 v[122:125], v2, s[40:41] offset:96
	v_mov_b32_e32 v228, 0
	v_mov_b32_e32 v229, 0
	v_mov_b32_e32 v230, 0
	v_mov_b32_e32 v231, 0
	v_mov_b32_e32 v232, 0
	v_mov_b32_e32 v233, 0
	v_mov_b32_e32 v234, 0
	v_mov_b32_e32 v235, 0
	v_mov_b32_e32 v236, 0
	v_mov_b32_e32 v237, 0
	v_mov_b32_e32 v238, 0
	v_mov_b32_e32 v239, 0
	v_mov_b32_e32 v240, 0
	v_mov_b32_e32 v241, 0
	v_mov_b32_e32 v242, 0
	v_mov_b32_e32 v243, 0
	v_mov_b32_e32 v16, v3
	v_mov_b32_e32 v17, v3
	v_lshlrev_b32_e32 v2, 10, v214
	v_lshlrev_b32_e32 v18, 4, v213
	v_mov_b32_e32 v4, v3
	v_mov_b32_e32 v5, v3
	v_mov_b32_e32 v6, v3
	v_mov_b32_e32 v7, v3
	v_mov_b32_e32 v8, v3
	v_mov_b32_e32 v9, v3
	v_mov_b32_e32 v10, v3
	v_mov_b32_e32 v11, v3
	v_mov_b32_e32 v12, v3
	v_mov_b32_e32 v13, v3
	v_mov_b32_e32 v14, v3
	v_mov_b32_e32 v15, v3
	v_add3_u32 v221, 0, v2, v18
	v_mov_b32_e32 v2, v3
	v_mov_b64_e32 v[32:33], v[16:17]
	v_mov_b64_e32 v[30:31], v[14:15]
	v_mov_b64_e32 v[28:29], v[12:13]
	v_mov_b64_e32 v[26:27], v[10:11]
	v_mov_b64_e32 v[24:25], v[8:9]
	v_mov_b64_e32 v[22:23], v[6:7]
	v_mov_b64_e32 v[20:21], v[4:5]
	v_mov_b64_e32 v[18:19], v[2:3]
	v_lshl_add_u64 v[34:35], v[194:195], 0, s[0:1]
	s_add_i32 s40, s58, 0x4000
	s_mov_b32 s41, m0
	s_mov_b32 m0, s40
	s_nop 0
	global_load_lds_dwordx4 v[34:35], off
	s_mov_b32 m0, s41
	s_waitcnt vmcnt(3) lgkmcnt(0)
	s_barrier
; __device__ __forceinline__ void qkt(f32x16&p0,f32x16&p1,const char*Kslot,const bf16x8*qr,const f32x16&negm,int r32,int hi){
;   const char*kb=Kslot+hi*1024+r32*16;
;   #pragma unroll
;   for(int d0=0;d0<4;++d0){
;     const bf16x8 b0=*reinterpret_cast<const bf16x8*>(kb+d0*2048);
;     const bf16x8 b1=*reinterpret_cast<const bf16x8*>(kb+d0*2048+512);
;     if(d0==0){p0=__builtin_amdgcn_mfma_f32_32x32x16_bf16(b0,qr[0],negm,0,0,0);p1=__builtin_amdgcn_mfma_f32_32x32x16_bf16(b1,qr[0],negm,0,0,0);}
;     else{p0=__builtin_amdgcn_mfma_f32_32x32x16_bf16(b0,qr[d0],p0,0,0,0);p1=__builtin_amdgcn_mfma_f32_32x32x16_bf16(b1,qr[d0],p1,0,0,0);}}
; }
; __device__ __forceinline__ void kload8(bf16x8*kf,lds_cptr kp){
;   kf[0]=*(const __attribute__((address_space(3))) bf16x8*)(kp);      kf[1]=*(const __attribute__((address_space(3))) bf16x8*)(kp+512);
;   kf[2]=*(const __attribute__((address_space(3))) bf16x8*)(kp+2048); kf[3]=*(const __attribute__((address_space(3))) bf16x8*)(kp+2560);
;   kf[4]=*(const __attribute__((address_space(3))) bf16x8*)(kp+4096); kf[5]=*(const __attribute__((address_space(3))) bf16x8*)(kp+4608);
;   kf[6]=*(const __attribute__((address_space(3))) bf16x8*)(kp+6144); kf[7]=*(const __attribute__((address_space(3))) bf16x8*)(kp+6656);
; }
; __device__ __forceinline__ void kload2(bf16x8*kf,lds_cptr kp,int j){ kf[2*j]=*(const __attribute__((address_space(3))) bf16x8*)(kp+j*2048); kf[2*j+1]=*(const __attribute__((address_space(3))) bf16x8*)(kp+j*2048+512); }
; __device__ __forceinline__ s16x4 vtr(lds_cptr p){ return __builtin_bit_cast(s16x4,__builtin_amdgcn_ds_read_tr16_b64_v4i16((__attribute__((address_space(3))) v4i16_t*)p)); }
; __device__ __forceinline__ float rowmax(const f32x16&p0,const f32x16&p1){
; template<int THRL> __device__ __forceinline__ void attn_unit(int b,int h,int qb,const bf16*Q,const bf16*__restrict__ K,const bf16*__restrict__ V,bf16*O,const unsigned*MASK,char*shm){
;     ...
;   f32x16 pA0,pA1,pB0,pB1;
;   int sl_prev=0,sl_cur=0,sl_next=SLOTB;
;     ...
;   DMA_K(2,2*SLOTB);
;   WAIT_BAR(3);
;   qkt(pA0,pA1,Kbase,qr,negm,r32,hi);asm volatile("s_nop 15\n\ts_nop 7":"+v"(pA0),"+v"(pA1));
;   START(pA0,pA1);
;   _Pragma("unroll") for(int r=0;r<16;++r)pA1[r]=__builtin_amdgcn_exp2f(pA1[r]);
;   _Pragma("unroll") for(int r=0;r<16;++r){pA0[r]=MASK1(pA0[r],wA,r);pA1[r]=MASK1(pA1[r],wA,16+r);}
	ds_read_b128 v[50:53], v221
	ds_read_b128 v[54:57], v221 offset:512
	s_mov_b32 s40, 0xf149f2ca
	s_waitcnt vmcnt(3) lgkmcnt(1)
	v_mfma_f32_32x32x16_bf16 v[34:49], v[50:53], v[138:141], v[18:33]
	v_bfe_i32 v70, v59, 3, 1
	v_bfe_i32 v71, v59, 4, 1
	v_bfe_i32 v72, v59, 5, 1
	v_bfe_i32 v73, v59, 6, 1
	v_bfe_i32 v74, v59, 7, 1
	v_bfe_i32 v75, v59, 8, 1
	v_bfe_i32 v76, v59, 9, 1
	s_waitcnt lgkmcnt(0)
	v_mfma_f32_32x32x16_bf16 v[18:33], v[54:57], v[138:141], v[18:33]
	ds_read_b128 v[50:53], v221 offset:2048
	ds_read_b128 v[54:57], v221 offset:2560
	v_bfe_i32 v77, v59, 10, 1
	v_bfe_i32 v78, v59, 11, 1
	v_bfe_i32 v79, v59, 12, 1
	v_bfe_i32 v80, v59, 13, 1
	v_bfe_i32 v81, v59, 14, 1
	v_bfe_i32 v82, v59, 15, 1
	s_waitcnt vmcnt(2) lgkmcnt(1)
	v_mfma_f32_32x32x16_bf16 v[34:49], v[50:53], v[134:137], v[34:49]
	s_lshl_b32 s5, s5, 2
	v_bfe_i32 v86, v59, 16, 1
	v_bfe_i32 v87, v59, 17, 1
	v_bfe_i32 v69, v59, 2, 1
	s_ashr_i32 s61, s4, 6
	s_add_i32 s57, s5, 0
	v_bfe_i32 v67, v59, 0, 1
	s_waitcnt lgkmcnt(0)
	v_mfma_f32_32x32x16_bf16 v[18:33], v[54:57], v[134:137], v[18:33]
	ds_read_b128 v[50:53], v221 offset:4096
	ds_read_b128 v[54:57], v221 offset:4608
	v_bfe_i32 v68, v59, 1, 1
	s_mov_b32 s92, 1
	s_mov_b32 s48, 0
	s_movk_i32 s60, 0x2000
	s_movk_i32 s62, 0x4000
	v_bfe_i32 v88, v59, 18, 1
	s_waitcnt vmcnt(1) lgkmcnt(1)
	v_mfma_f32_32x32x16_bf16 v[34:49], v[50:53], v[126:129], v[34:49]
	ds_read_b128 v[50:53], v221 offset:6144
	v_bfe_i32 v89, v59, 19, 1
	v_bfe_i32 v90, v59, 20, 1
	v_bfe_i32 v91, v59, 21, 1
	v_bfe_i32 v92, v59, 22, 1
	v_bfe_i32 v93, v59, 23, 1
	v_bfe_i32 v94, v59, 24, 1
	s_waitcnt lgkmcnt(1)
	v_mfma_f32_32x32x16_bf16 v[18:33], v[54:57], v[126:129], v[18:33]
	ds_read_b128 v[54:57], v221 offset:6656
	v_bfe_i32 v95, v59, 25, 1
	v_bfe_i32 v96, v59, 26, 1
	v_bfe_i32 v97, v59, 27, 1
	v_bfe_i32 v98, v59, 28, 1
	v_bfe_i32 v99, v59, 29, 1
	v_bfe_i32 v100, v59, 30, 1
	s_waitcnt vmcnt(0) lgkmcnt(1)
	v_mfma_f32_32x32x16_bf16 v[34:49], v[50:53], v[122:125], v[34:49]
	v_lshlrev_b32_e32 v50, 1, v58
	v_lshlrev_b32_e32 v51, 4, v58
	v_and_b32_e32 v217, 32, v50
	v_and_b32_e32 v50, 0xc0, v51
	v_lshl_or_b32 v216, v214, 8, v50
	v_add_u32_e32 v50, 0, v217
	v_add3_u32 v220, v50, v215, v216
	s_waitcnt lgkmcnt(0)
	v_mfma_f32_32x32x16_bf16 v[18:33], v[54:57], v[122:125], v[18:33]
	s_nop 15
	s_nop 7
	s_nop 0
	v_max3_f32 v50, v34, v35, v18
	v_max3_f32 v51, v36, v37, v19
	s_nop 0
	v_max3_f32 v50, v50, v20, v21
	v_max3_f32 v51, v51, v40, v41
	s_nop 0
	v_max3_f32 v50, v50, v38, v39
	v_max3_f32 v51, v51, v24, v25
	s_nop 0
	v_max3_f32 v50, v50, v22, v23
	v_max3_f32 v51, v51, v44, v45
	s_nop 0
	v_max3_f32 v50, v50, v42, v43
	v_max3_f32 v51, v51, v28, v29
	s_nop 0
	v_max3_f32 v50, v50, v26, v27
	v_max3_f32 v51, v51, v48, v49
	s_nop 0
	v_max3_f32 v50, v50, v46, v47
	v_max3_f32 v51, v51, v32, v33
	s_nop 0
	v_max3_f32 v50, v50, v30, v31
	s_nop 0
	v_max_f32_e32 v50, v50, v51
	s_nop 0
	v_mov_b32_e32 v51, v50
	s_nop 1
	v_permlane32_swap_b32_e32 v50, v51
	v_max_f32_e32 v50, v50, v51
	s_nop 0
	v_cmp_lt_f32_e32 vcc, s40, v50
	v_cmp_gt_u32_e64 s[40:41], 32, v1
	s_nop 0
	v_cndmask_b32_e32 v50, 0, v50, vcc
	v_sub_f32_e32 v18, v18, v50
	v_sub_f32_e32 v19, v19, v50
	v_sub_f32_e32 v52, v36, v50
	v_sub_f32_e32 v53, v37, v50
	v_sub_f32_e32 v54, v38, v50
	v_sub_f32_e32 v55, v39, v50
	v_sub_f32_e32 v56, v40, v50
	v_sub_f32_e32 v57, v41, v50
	v_sub_f32_e32 v58, v42, v50
	v_sub_f32_e32 v60, v43, v50
	v_sub_f32_e32 v61, v44, v50
	v_sub_f32_e32 v62, v45, v50
	v_sub_f32_e32 v63, v46, v50
	v_sub_f32_e32 v64, v47, v50
	v_sub_f32_e32 v65, v48, v50
	v_sub_f32_e32 v66, v49, v50
	s_nop 0
	v_exp_f32_e32 v52, v52
	v_exp_f32_e32 v53, v53
	v_exp_f32_e32 v54, v54
	v_exp_f32_e32 v55, v55
	v_exp_f32_e32 v56, v56
	v_exp_f32_e32 v57, v57
	v_exp_f32_e32 v58, v58
	v_exp_f32_e32 v60, v60
	v_exp_f32_e32 v61, v61
	v_exp_f32_e32 v62, v62
	v_exp_f32_e32 v63, v63
	v_exp_f32_e32 v64, v64
	v_exp_f32_e32 v65, v65
	v_exp_f32_e32 v66, v66
	v_exp_f32_e32 v18, v18
	v_exp_f32_e32 v19, v19
	v_add_f32_e32 v219, v3, v50
	v_sub_f32_e32 v34, v34, v50
	v_sub_f32_e32 v35, v35, v50
	v_sub_f32_e32 v20, v20, v50
	v_sub_f32_e32 v21, v21, v50
	v_sub_f32_e32 v22, v22, v50
	s_nop 0
	v_xor_b32_e32 v36, 0x80000000, v219
	v_sub_f32_e32 v23, v23, v50
	v_sub_f32_e32 v24, v24, v50
	v_sub_f32_e32 v25, v25, v50
	v_sub_f32_e32 v26, v26, v50
	v_sub_f32_e32 v27, v27, v50
	v_sub_f32_e32 v28, v28, v50
	v_sub_f32_e32 v29, v29, v50
	v_sub_f32_e32 v30, v30, v50
	v_sub_f32_e32 v31, v31, v50
	v_sub_f32_e32 v32, v32, v50
	v_sub_f32_e32 v33, v33, v50
	v_mov_b32_e32 v37, v36
	v_mov_b32_e32 v38, v36
	v_mov_b32_e32 v39, v36
	v_mov_b32_e32 v40, v36
	v_mov_b32_e32 v41, v36
	v_mov_b32_e32 v42, v36
	v_mov_b32_e32 v43, v36
	v_mov_b32_e32 v44, v36
	v_mov_b32_e32 v45, v36
	v_mov_b32_e32 v46, v36
	v_mov_b32_e32 v47, v36
	v_mov_b32_e32 v48, v36
	v_mov_b32_e32 v49, v36
	v_mov_b32_e32 v50, v36
	v_mov_b32_e32 v51, v36
	s_waitcnt vmcnt(0) lgkmcnt(0)
	s_barrier
; #define MASK1(p,w,e) ({ unsigned m_; asm("v_bfe_i32 %0, %1, %2, 1":"=v"(m_):"v"(w),"n"(e)); __uint_as_float(__float_as_uint(p)&m_); })
; #define WAIT_BAR(N) asm volatile("s_waitcnt vmcnt(" #N ") lgkmcnt(0)\n\ts_barrier":::"memory")
;   #define DMA_K(t,slot) glds16(ksrc+(long)(t)*KVBLK*DM,(unsigned)__builtin_amdgcn_readfirstlane(kdst+(slot)))
;   #define DMA_V(t,slot) glds16(vsrc+(long)(t)*KVBLK*DM,(unsigned)__builtin_amdgcn_readfirstlane(vdst+(slot)))
;   #define ROT() do{sl_prev=sl_cur;sl_cur=sl_next;sl_next=(sl_next==(NSLOT-1)*SLOTB)?0:sl_next+SLOTB;}while(0)
; template<int THRL> __device__ __forceinline__ void attn_unit(int b,int h,int qb,const bf16*Q,const bf16*__restrict__ K,const bf16*__restrict__ V,bf16*O,const unsigned*MASK,char*shm){
;     ...
;   _Pragma("unroll") for(int r=0;r<16;++r){pA0[r]=MASK1(pA0[r],wA,r);pA1[r]=MASK1(pA1[r],wA,16+r);}
;   WAIT_BAR(0);
;   DMA_K(3,0);DMA_V(1,SLOTB);
;   ROT();
;   kload8(kf,kp0+sl_cur);
;   WAIT_BAR(2);
;   s16x4 vlo[8],vhi[8]; u32x4 pw0,pw1,pw2,pw3;
	v_and_b32_e32 v83, v82, v66
	v_and_b32_e32 v82, v81, v65
	v_and_b32_e32 v81, v80, v64
	v_and_b32_e32 v80, v79, v63
	v_and_b32_e32 v79, v78, v62
	v_and_b32_e32 v78, v77, v61
	v_and_b32_e32 v77, v76, v60
	v_and_b32_e32 v76, v75, v58
	v_and_b32_e32 v75, v74, v57
	v_and_b32_e32 v74, v73, v56
	v_and_b32_e32 v73, v72, v55
	v_and_b32_e32 v72, v71, v54
	v_and_b32_e32 v71, v70, v53
	v_and_b32_e32 v70, v69, v52
	v_and_b32_e32 v53, v87, v19
	v_and_b32_e32 v52, v86, v18
	v_lshl_add_u64 v[18:19], v[194:195], 0, s[82:83]
	s_mov_b32 s4, m0
	s_mov_b32 m0, s58
	s_nop 0
	global_load_lds_dwordx4 v[18:19], off
	s_mov_b32 m0, s4
	v_lshl_add_u64 v[18:19], v[208:209], 0, s[36:37]
	s_add_i32 s4, s58, 0x8000
	s_mov_b32 s5, m0
	s_mov_b32 m0, s4
	s_nop 0
	global_load_lds_dwordx4 v[18:19], off
	s_mov_b32 m0, s5
	ds_read_b128 v[178:181], v221 offset:8192
	ds_read_b128 v[170:173], v221 offset:8704
	ds_read_b128 v[174:177], v221 offset:10240
	ds_read_b128 v[162:165], v221 offset:10752
	ds_read_b128 v[166:169], v221 offset:12288
	ds_read_b128 v[154:157], v221 offset:12800
	ds_read_b128 v[158:161], v221 offset:14336
	ds_read_b128 v[150:153], v221 offset:14848
	v_exp_f32_e32 v34, v34
	v_exp_f32_e32 v35, v35
	v_exp_f32_e32 v20, v20
	v_exp_f32_e32 v21, v21
	v_exp_f32_e32 v22, v22
	v_exp_f32_e32 v23, v23
	v_exp_f32_e32 v24, v24
	v_exp_f32_e32 v25, v25
	v_exp_f32_e32 v26, v26
	v_exp_f32_e32 v27, v27
	v_exp_f32_e32 v28, v28
	v_exp_f32_e32 v29, v29
	v_exp_f32_e32 v30, v30
	v_exp_f32_e32 v31, v31
	v_exp_f32_e32 v32, v32
	v_exp_f32_e32 v33, v33
	s_waitcnt vmcnt(2) lgkmcnt(0)
	s_barrier
	v_and_b32_e32 v69, v68, v35
	v_and_b32_e32 v68, v67, v34
	v_bfe_i32 v34, v59, 31, 1
	v_and_b32_e32 v66, v100, v32
	v_and_b32_e32 v67, v34, v33
	v_and_b32_e32 v65, v99, v31
	v_and_b32_e32 v64, v98, v30
	v_and_b32_e32 v63, v97, v29
	v_and_b32_e32 v62, v96, v28
	v_and_b32_e32 v61, v95, v27
	v_and_b32_e32 v60, v94, v26
	v_and_b32_e32 v59, v93, v25
	v_and_b32_e32 v58, v92, v24
	v_and_b32_e32 v57, v91, v23
	v_and_b32_e32 v56, v90, v22
	v_and_b32_e32 v55, v89, v21
	v_and_b32_e32 v54, v88, v20
	s_cmp_lt_i32 s61, 7
	s_cbranch_scc1 .LBB0_1287
	s_mov_b64 s[4:5], 0x50000
	v_lshlrev_b32_e32 v18, 4, v214
	v_lshl_add_u64 v[188:189], v[194:195], 0, s[4:5]
	s_mov_b64 s[4:5], 0x300
	v_mov_b64_e32 v[34:35], v[16:17]
	v_lshl_add_u64 v[192:193], v[84:85], 0, s[4:5]
	v_add_u32_e32 v85, s57, v18
	v_mov_b64_e32 v[32:33], v[14:15]
	v_mov_b64_e32 v[30:31], v[12:13]
	v_mov_b64_e32 v[28:29], v[10:11]
	v_mov_b64_e32 v[26:27], v[8:9]
	v_mov_b64_e32 v[24:25], v[6:7]
	v_mov_b64_e32 v[22:23], v[4:5]
	v_mov_b64_e32 v[20:21], v[2:3]
	v_mov_b64_e32 v[18:19], v[16:17]
	s_add_i32 s46, s61, -5
	v_lshl_add_u32 v210, v213, 2, s57
	v_lshl_add_u64 v[190:191], v[208:209], 0, s[82:83]
	s_mov_b32 s4, 0
	s_movk_i32 s48, 0x4000
	s_movk_i32 s47, 0x2000
	v_mov_b32_e32 v84, 0
	v_mov_b64_e32 v[16:17], v[14:15]
	v_mov_b64_e32 v[14:15], v[12:13]
	v_mov_b64_e32 v[12:13], v[10:11]
	v_mov_b64_e32 v[10:11], v[8:9]
	v_mov_b64_e32 v[8:9], v[6:7]
	v_mov_b64_e32 v[6:7], v[4:5]
	v_mov_b64_e32 v[4:5], v[2:3]
.LBB0_1273:
	s_movk_i32 s42, 0xff00
	s_mov_b32 s43, -1
	v_lshl_add_u64 v[86:87], v[192:193], 0, s[42:43]
	global_load_dword v2, v[86:87], off
	v_add_u32_e32 v255, s4, v220
	ds_read_b64_tr_b16 v[182:183], v255 offset:24576
	ds_read_b64_tr_b16 v[184:185], v255 offset:25088
	s_waitcnt lgkmcnt(9)
	v_mfma_f32_32x32x16_bf16 v[102:117], v[178:181], v[138:141], v[36:51]
	v_cvt_pk_bf16_f32 v146, v68, v69
	v_cvt_pk_bf16_f32 v147, v70, v71
	ds_read_b64_tr_b16 v[178:179], v255 offset:28672
	ds_read_b64_tr_b16 v[180:181], v255 offset:29184
	s_waitcnt lgkmcnt(10)
	v_mfma_f32_32x32x16_bf16 v[86:101], v[170:173], v[138:141], v[36:51]
	v_cvt_pk_bf16_f32 v148, v72, v73
	v_cvt_pk_bf16_f32 v149, v74, v75
	ds_read_b64_tr_b16 v[170:171], v255 offset:25600
	ds_read_b64_tr_b16 v[172:173], v255 offset:26112
	s_waitcnt lgkmcnt(11)
	v_mfma_f32_32x32x16_bf16 v[102:117], v[174:177], v[134:137], v[102:117]
	v_cvt_pk_bf16_f32 v142, v76, v77
	v_cvt_pk_bf16_f32 v143, v78, v79
	ds_read_b64_tr_b16 v[76:77], v255 offset:29696
	ds_read_b64_tr_b16 v[78:79], v255 offset:30208
	s_waitcnt lgkmcnt(12)
	v_mfma_f32_32x32x16_bf16 v[86:101], v[162:165], v[134:137], v[86:101]
	v_cvt_pk_bf16_f32 v144, v80, v81
	v_cvt_pk_bf16_f32 v145, v82, v83
	ds_read_b64_tr_b16 v[72:73], v255 offset:26624
	ds_read_b64_tr_b16 v[74:75], v255 offset:27136
	s_waitcnt lgkmcnt(13)
	v_mfma_f32_32x32x16_bf16 v[102:117], v[166:169], v[126:129], v[102:117]
	v_cvt_pk_bf16_f32 v130, v52, v53
	v_cvt_pk_bf16_f32 v131, v54, v55
	ds_read_b64_tr_b16 v[68:69], v255 offset:30720
	ds_read_b64_tr_b16 v[70:71], v255 offset:31232
	s_waitcnt lgkmcnt(14)
	v_mfma_f32_32x32x16_bf16 v[86:101], v[154:157], v[126:129], v[86:101]
	v_cvt_pk_bf16_f32 v132, v56, v57
	v_cvt_pk_bf16_f32 v133, v58, v59
	ds_read_b64_tr_b16 v[56:57], v255 offset:27648
	ds_read_b64_tr_b16 v[58:59], v255 offset:28160
	s_waitcnt lgkmcnt(14)
	v_mfma_f32_32x32x16_bf16 v[102:117], v[158:161], v[122:125], v[102:117]
	v_cvt_pk_bf16_f32 v118, v60, v61
	v_cvt_pk_bf16_f32 v119, v62, v63
	ds_read_b64_tr_b16 v[52:53], v255 offset:31744
	ds_read_b64_tr_b16 v[54:55], v255 offset:32256
	v_mfma_f32_32x32x16_bf16 v[86:101], v[150:153], v[122:125], v[86:101]
	v_cvt_pk_bf16_f32 v120, v64, v65
	v_cvt_pk_bf16_f32 v121, v66, v67
	ds_read_b128 v[80:83], v225 offset:51200
	v_lshl_add_u64 v[60:61], v[188:189], 0, s[86:87]
	s_add_i32 s4, s47, s58
	s_mov_b32 s5, m0
	s_mov_b32 m0, s4
	s_nop 0
	global_load_lds_dwordx4 v[60:61], off
	s_mov_b32 m0, s5
	v_lshl_add_u64 v[60:61], v[190:191], 0, s[86:87]
	s_add_i32 s4, s48, s59
	s_mov_b32 s5, m0
	s_mov_b32 m0, s4
	s_nop 0
	global_load_lds_dwordx4 v[60:61], off
	s_mov_b32 m0, s5
	v_max_f32_e32 v60, v103, v103
	v_max_f32_e32 v61, v102, v102
	v_max_f32_e32 v60, v61, v60
	v_max3_f32 v61, v104, v105, v87
	v_max3_f32 v60, v60, v86, v88
	v_max3_f32 v60, v60, v89, v106
	v_max3_f32 v61, v61, v108, v109
	v_max3_f32 v60, v60, v107, v90
	v_max3_f32 v61, v61, v92, v93
	v_max3_f32 v60, v60, v91, v110
	v_max3_f32 v61, v61, v112, v113
	v_max3_f32 v60, v60, v111, v94
	v_max3_f32 v61, v61, v96, v97
	v_max3_f32 v60, v60, v95, v114
	v_max3_f32 v61, v61, v116, v117
	v_max3_f32 v60, v60, v115, v98
	v_max3_f32 v61, v61, v100, v101
	v_max3_f32 v60, v60, v99, v61
	v_mov_b32_e32 v61, v60
	s_nop 1
	v_permlane32_swap_b32_e32 v60, v61
	v_max_f32_e32 v61, v61, v61
	v_max_f32_e32 v60, v60, v60
	v_max_f32_e32 v60, v60, v61
	v_cmp_lt_f32_e32 vcc, s14, v60
	s_cmp_lg_u64 vcc, 0
	s_cselect_b64 s[42:43], -1, 0
	s_cbranch_vccnz .LBB0_1281
.LBB0_1274:
	s_waitcnt lgkmcnt(0)
	v_and_b32_e32 v146, v146, v80
	v_and_b32_e32 v147, v147, v81
	v_and_b32_e32 v148, v148, v82
	v_and_b32_e32 v149, v149, v83
	ds_read_b128 v[80:83], v226 offset:51200
	s_waitcnt lgkmcnt(14)
	v_mfma_f32_32x32x16_bf16 v[20:35], v[146:149], v[182:185], v[20:35]
	v_exp_f32_e32 v102, v102
	v_exp_f32_e32 v103, v103
	v_exp_f32_e32 v104, v104
	v_exp_f32_e32 v105, v105
	s_waitcnt lgkmcnt(12)
	v_mfma_f32_32x32x16_bf16 v[4:19], v[146:149], v[178:181], v[4:19]
	v_mfma_f32_32x32x16_bf16 v[228:243], v[146:149], v[204:207], v[228:243]
	v_exp_f32_e32 v106, v106
	v_exp_f32_e32 v107, v107
	v_exp_f32_e32 v108, v108
	v_exp_f32_e32 v109, v109
	s_waitcnt lgkmcnt(0)
	v_and_b32_e32 v142, v142, v80
	v_and_b32_e32 v143, v143, v81
	v_and_b32_e32 v144, v144, v82
	v_and_b32_e32 v145, v145, v83
	ds_read_b128 v[80:83], v248 offset:51200
	v_add_u32_e32 v64, s48, v221
	ds_read_b128 v[60:63], v64
	ds_read_b128 v[150:153], v64 offset:512
	s_waitcnt lgkmcnt(12)
	v_mfma_f32_32x32x16_bf16 v[20:35], v[142:145], v[170:173], v[20:35]
	v_exp_f32_e32 v110, v110
	v_exp_f32_e32 v111, v111
	v_exp_f32_e32 v112, v112
	v_exp_f32_e32 v113, v113
	ds_read_b128 v[174:177], v64 offset:2048
	ds_read_b128 v[162:165], v64 offset:2560
	s_waitcnt lgkmcnt(12)
	v_mfma_f32_32x32x16_bf16 v[4:19], v[142:145], v[76:79], v[4:19]
	v_mfma_f32_32x32x16_bf16 v[228:243], v[142:145], v[204:207], v[228:243]
	v_exp_f32_e32 v114, v114
	v_exp_f32_e32 v115, v115
	v_exp_f32_e32 v116, v116
	v_exp_f32_e32 v117, v117
	s_waitcnt lgkmcnt(4)
	v_and_b32_e32 v130, v130, v80
	v_and_b32_e32 v131, v131, v81
	v_and_b32_e32 v132, v132, v82
	v_and_b32_e32 v133, v133, v83
	ds_read_b128 v[80:83], v249 offset:51200
	ds_read_b128 v[170:173], v64 offset:4096
	ds_read_b128 v[158:161], v64 offset:4608
	s_waitcnt lgkmcnt(12)
	v_mfma_f32_32x32x16_bf16 v[20:35], v[130:133], v[72:75], v[20:35]
	v_exp_f32_e32 v86, v86
	v_exp_f32_e32 v87, v87
	v_exp_f32_e32 v88, v88
	v_exp_f32_e32 v89, v89
	ds_read_b128 v[166:169], v64 offset:6144
	ds_read_b128 v[154:157], v64 offset:6656
	s_waitcnt lgkmcnt(12)
	v_mfma_f32_32x32x16_bf16 v[4:19], v[130:133], v[68:71], v[4:19]
	v_mfma_f32_32x32x16_bf16 v[228:243], v[130:133], v[204:207], v[228:243]
	v_exp_f32_e32 v90, v90
	v_exp_f32_e32 v91, v91
	v_exp_f32_e32 v92, v92
	v_exp_f32_e32 v93, v93
	s_waitcnt lgkmcnt(4)
	v_and_b32_e32 v118, v118, v80
	v_and_b32_e32 v119, v119, v81
	v_and_b32_e32 v120, v120, v82
	v_and_b32_e32 v121, v121, v83
	s_nop 0
	s_waitcnt lgkmcnt(10)
	v_mfma_f32_32x32x16_bf16 v[20:35], v[118:121], v[56:59], v[20:35]
	v_exp_f32_e32 v94, v94
	v_exp_f32_e32 v95, v95
	v_exp_f32_e32 v96, v96
	v_exp_f32_e32 v97, v97
	s_waitcnt lgkmcnt(8)
	v_mfma_f32_32x32x16_bf16 v[4:19], v[118:121], v[52:55], v[4:19]
	v_mfma_f32_32x32x16_bf16 v[228:243], v[118:121], v[204:207], v[228:243]
	v_exp_f32_e32 v98, v98
	v_exp_f32_e32 v99, v99
	v_exp_f32_e32 v100, v100
	v_exp_f32_e32 v101, v101
	v_lshlrev_b32_sdwa v225, s32, v218 dst_sel:DWORD dst_unused:UNUSED_PAD src0_sel:DWORD src1_sel:BYTE_0
	v_lshlrev_b32_sdwa v226, s32, v218 dst_sel:DWORD dst_unused:UNUSED_PAD src0_sel:DWORD src1_sel:BYTE_1
	v_lshlrev_b32_sdwa v248, s32, v218 dst_sel:DWORD dst_unused:UNUSED_PAD src0_sel:DWORD src1_sel:BYTE_2
	v_lshlrev_b32_sdwa v249, s32, v218 dst_sel:DWORD dst_unused:UNUSED_PAD src0_sel:DWORD src1_sel:BYTE_3
	s_waitcnt vmcnt(2) lgkmcnt(0)
	s_barrier
	s_andn2_b64 vcc, exec, s[42:43]
	s_cbranch_vccnz .LBB0_1276
	s_waitcnt lgkmcnt(0)
	ds_read_b128 v[52:55], v85 offset:49248
	ds_read_b128 v[56:59], v85 offset:49216
	ds_read_b128 v[64:67], v85 offset:49184
	ds_read_b128 v[68:71], v85 offset:49152
	s_waitcnt lgkmcnt(3)
	v_pk_mul_f32 v[32:33], v[32:33], v[52:53]
	s_waitcnt lgkmcnt(2)
	v_pk_mul_f32 v[28:29], v[28:29], v[56:57]
	s_waitcnt lgkmcnt(1)
	v_pk_mul_f32 v[24:25], v[24:25], v[64:65]
	v_pk_mul_f32 v[34:35], v[34:35], v[54:55]
	v_pk_mul_f32 v[30:31], v[30:31], v[58:59]
	v_pk_mul_f32 v[26:27], v[26:27], v[66:67]
	s_waitcnt lgkmcnt(0)
	v_pk_mul_f32 v[22:23], v[22:23], v[70:71]
	v_pk_mul_f32 v[20:21], v[20:21], v[68:69]
	v_pk_mul_f32 v[16:17], v[16:17], v[52:53]
	v_pk_mul_f32 v[12:13], v[12:13], v[56:57]
	v_pk_mul_f32 v[8:9], v[8:9], v[64:65]
	v_pk_mul_f32 v[18:19], v[18:19], v[54:55]
	v_pk_mul_f32 v[14:15], v[14:15], v[58:59]
	v_pk_mul_f32 v[10:11], v[10:11], v[66:67]
	v_pk_mul_f32 v[6:7], v[6:7], v[70:71]
	v_pk_mul_f32 v[4:5], v[4:5], v[68:69]
	v_pk_mul_f32 v[240:241], v[240:241], v[52:53]
	v_pk_mul_f32 v[236:237], v[236:237], v[56:57]
	v_pk_mul_f32 v[232:233], v[232:233], v[64:65]
	v_pk_mul_f32 v[242:243], v[242:243], v[54:55]
	v_pk_mul_f32 v[238:239], v[238:239], v[58:59]
	v_pk_mul_f32 v[234:235], v[234:235], v[66:67]
	v_pk_mul_f32 v[230:231], v[230:231], v[70:71]
	v_pk_mul_f32 v[228:229], v[228:229], v[68:69]
.LBB0_1276:
	s_add_i32 s4, s48, 0x2000
	s_cmpk_lg_i32 s48, 0x4000
	s_cselect_b32 s60, s4, 0
	global_load_dword v218, v[192:193], off
	v_add_u32_e32 v255, s47, v220
	ds_read_b64_tr_b16 v[182:183], v255 offset:24576
	ds_read_b64_tr_b16 v[184:185], v255 offset:25088
	s_waitcnt lgkmcnt(9)
	v_mfma_f32_32x32x16_bf16 v[68:83], v[60:63], v[138:141], v[36:51]
	v_cvt_pk_bf16_f32 v146, v102, v103
	v_cvt_pk_bf16_f32 v147, v104, v105
	ds_read_b64_tr_b16 v[178:179], v255 offset:28672
	ds_read_b64_tr_b16 v[180:181], v255 offset:29184
	s_waitcnt lgkmcnt(10)
	v_mfma_f32_32x32x16_bf16 v[52:67], v[150:153], v[138:141], v[36:51]
	v_cvt_pk_bf16_f32 v148, v106, v107
	v_cvt_pk_bf16_f32 v149, v108, v109
	ds_read_b64_tr_b16 v[150:151], v255 offset:25600
	ds_read_b64_tr_b16 v[152:153], v255 offset:26112
	s_waitcnt lgkmcnt(11)
	v_mfma_f32_32x32x16_bf16 v[68:83], v[174:177], v[134:137], v[68:83]
	v_cvt_pk_bf16_f32 v142, v110, v111
	v_cvt_pk_bf16_f32 v143, v112, v113
	ds_read_b64_tr_b16 v[110:111], v255 offset:29696
	ds_read_b64_tr_b16 v[112:113], v255 offset:30208
	s_waitcnt lgkmcnt(12)
	v_mfma_f32_32x32x16_bf16 v[52:67], v[162:165], v[134:137], v[52:67]
	v_cvt_pk_bf16_f32 v144, v114, v115
	v_cvt_pk_bf16_f32 v145, v116, v117
	ds_read_b64_tr_b16 v[106:107], v255 offset:26624
	ds_read_b64_tr_b16 v[108:109], v255 offset:27136
	s_waitcnt lgkmcnt(13)
	v_mfma_f32_32x32x16_bf16 v[68:83], v[170:173], v[126:129], v[68:83]
	v_cvt_pk_bf16_f32 v130, v86, v87
	v_cvt_pk_bf16_f32 v131, v88, v89
	ds_read_b64_tr_b16 v[102:103], v255 offset:30720
	ds_read_b64_tr_b16 v[104:105], v255 offset:31232
	s_waitcnt lgkmcnt(14)
	v_mfma_f32_32x32x16_bf16 v[52:67], v[158:161], v[126:129], v[52:67]
	v_cvt_pk_bf16_f32 v132, v90, v91
	v_cvt_pk_bf16_f32 v133, v92, v93
	ds_read_b64_tr_b16 v[90:91], v255 offset:27648
	ds_read_b64_tr_b16 v[92:93], v255 offset:28160
	s_waitcnt lgkmcnt(14)
	v_mfma_f32_32x32x16_bf16 v[68:83], v[166:169], v[122:125], v[68:83]
	v_cvt_pk_bf16_f32 v118, v94, v95
	v_cvt_pk_bf16_f32 v119, v96, v97
	ds_read_b64_tr_b16 v[86:87], v255 offset:31744
	ds_read_b64_tr_b16 v[88:89], v255 offset:32256
	v_mfma_f32_32x32x16_bf16 v[52:67], v[154:157], v[122:125], v[52:67]
	v_cvt_pk_bf16_f32 v120, v98, v99
	v_cvt_pk_bf16_f32 v121, v100, v101
	ds_read_b128 v[114:117], v225 offset:51200
	v_max_f32_e32 v95, v69, v69
	v_max_f32_e32 v96, v68, v68
	v_max_f32_e32 v95, v96, v95
	s_nop 3
	v_max3_f32 v96, v70, v71, v53
	v_max3_f32 v95, v95, v52, v54
	v_max3_f32 v95, v95, v55, v72
	v_max3_f32 v96, v96, v74, v75
	v_max3_f32 v95, v95, v73, v56
	v_max3_f32 v96, v96, v58, v59
	v_max3_f32 v95, v95, v57, v76
	v_max3_f32 v96, v96, v78, v79
	v_max3_f32 v95, v95, v77, v60
	v_max3_f32 v96, v96, v62, v63
	v_max3_f32 v95, v95, v61, v80
	v_max3_f32 v96, v96, v82, v83
	v_max3_f32 v95, v95, v81, v64
	v_max3_f32 v96, v96, v66, v67
	v_max3_f32 v94, v95, v65, v96
	v_mov_b32_e32 v95, v94
	s_nop 1
	v_permlane32_swap_b32_e32 v94, v95
	v_max_f32_e32 v95, v95, v95
	v_max_f32_e32 v94, v94, v94
	s_add_i32 s4, s48, s58
	s_mov_b32 s5, m0
	s_mov_b32 m0, s4
	s_nop 0
	global_load_lds_dwordx4 v[188:189], off
	s_mov_b32 m0, s5
	v_max_f32_e32 v94, v94, v95
	s_add_i32 s4, s60, s59
	s_mov_b32 s5, m0
	s_mov_b32 m0, s4
	s_nop 0
	global_load_lds_dwordx4 v[190:191], off
	s_mov_b32 m0, s5
	v_cmp_lt_f32_e32 vcc, s14, v94
	s_cmp_lg_u64 vcc, 0
	s_cselect_b64 s[42:43], -1, 0
	s_cbranch_vccnz .LBB0_1284
.LBB0_1277:
	s_waitcnt lgkmcnt(0)
	v_and_b32_e32 v146, v146, v114
	v_and_b32_e32 v147, v147, v115
	v_and_b32_e32 v148, v148, v116
	v_and_b32_e32 v149, v149, v117
	ds_read_b128 v[114:117], v226 offset:51200
	s_waitcnt lgkmcnt(14)
	v_mfma_f32_32x32x16_bf16 v[20:35], v[146:149], v[182:185], v[20:35]
	v_exp_f32_e32 v68, v68
	v_exp_f32_e32 v69, v69
	v_exp_f32_e32 v70, v70
	v_exp_f32_e32 v71, v71
	s_waitcnt lgkmcnt(12)
	v_mfma_f32_32x32x16_bf16 v[4:19], v[146:149], v[178:181], v[4:19]
	v_mfma_f32_32x32x16_bf16 v[228:243], v[146:149], v[204:207], v[228:243]
	v_exp_f32_e32 v72, v72
	v_exp_f32_e32 v73, v73
	v_exp_f32_e32 v74, v74
	v_exp_f32_e32 v75, v75
	s_waitcnt lgkmcnt(0)
	v_and_b32_e32 v142, v142, v114
	v_and_b32_e32 v143, v143, v115
	v_and_b32_e32 v144, v144, v116
	v_and_b32_e32 v145, v145, v117
	ds_read_b128 v[114:117], v248 offset:51200
	v_add_u32_e32 v94, s60, v221
	ds_read_b128 v[178:181], v94
	ds_read_b128 v[170:173], v94 offset:512
	s_waitcnt lgkmcnt(12)
	v_mfma_f32_32x32x16_bf16 v[20:35], v[142:145], v[150:153], v[20:35]
	v_exp_f32_e32 v76, v76
	v_exp_f32_e32 v77, v77
	v_exp_f32_e32 v78, v78
	v_exp_f32_e32 v79, v79
	ds_read_b128 v[174:177], v94 offset:2048
	ds_read_b128 v[162:165], v94 offset:2560
	s_waitcnt lgkmcnt(12)
	v_mfma_f32_32x32x16_bf16 v[4:19], v[142:145], v[110:113], v[4:19]
	v_mfma_f32_32x32x16_bf16 v[228:243], v[142:145], v[204:207], v[228:243]
	v_exp_f32_e32 v80, v80
	v_exp_f32_e32 v81, v81
	v_exp_f32_e32 v82, v82
	v_exp_f32_e32 v83, v83
	s_waitcnt lgkmcnt(4)
	v_and_b32_e32 v130, v130, v114
	v_and_b32_e32 v131, v131, v115
	v_and_b32_e32 v132, v132, v116
	v_and_b32_e32 v133, v133, v117
	ds_read_b128 v[114:117], v249 offset:51200
	ds_read_b128 v[166:169], v94 offset:4096
	ds_read_b128 v[154:157], v94 offset:4608
	s_waitcnt lgkmcnt(12)
	v_mfma_f32_32x32x16_bf16 v[20:35], v[130:133], v[106:109], v[20:35]
	v_exp_f32_e32 v52, v52
	v_exp_f32_e32 v53, v53
	v_exp_f32_e32 v54, v54
	v_exp_f32_e32 v55, v55
	ds_read_b128 v[158:161], v94 offset:6144
	ds_read_b128 v[150:153], v94 offset:6656
	s_waitcnt lgkmcnt(12)
	v_mfma_f32_32x32x16_bf16 v[4:19], v[130:133], v[102:105], v[4:19]
	v_mfma_f32_32x32x16_bf16 v[228:243], v[130:133], v[204:207], v[228:243]
	v_exp_f32_e32 v56, v56
	v_exp_f32_e32 v57, v57
	v_exp_f32_e32 v58, v58
	v_exp_f32_e32 v59, v59
	s_waitcnt lgkmcnt(4)
	v_and_b32_e32 v118, v118, v114
	v_and_b32_e32 v119, v119, v115
	v_and_b32_e32 v120, v120, v116
	v_and_b32_e32 v121, v121, v117
	s_nop 0
	s_waitcnt lgkmcnt(10)
	v_mfma_f32_32x32x16_bf16 v[20:35], v[118:121], v[90:93], v[20:35]
	v_exp_f32_e32 v60, v60
	v_exp_f32_e32 v61, v61
	v_exp_f32_e32 v62, v62
	v_exp_f32_e32 v63, v63
	s_waitcnt lgkmcnt(8)
	v_mfma_f32_32x32x16_bf16 v[4:19], v[118:121], v[86:89], v[4:19]
	v_mfma_f32_32x32x16_bf16 v[228:243], v[118:121], v[204:207], v[228:243]
	v_exp_f32_e32 v64, v64
	v_exp_f32_e32 v65, v65
	v_exp_f32_e32 v66, v66
	v_exp_f32_e32 v67, v67
	v_lshlrev_b32_sdwa v225, s32, v2 dst_sel:DWORD dst_unused:UNUSED_PAD src0_sel:DWORD src1_sel:BYTE_0
	v_lshlrev_b32_sdwa v226, s32, v2 dst_sel:DWORD dst_unused:UNUSED_PAD src0_sel:DWORD src1_sel:BYTE_1
	v_lshlrev_b32_sdwa v248, s32, v2 dst_sel:DWORD dst_unused:UNUSED_PAD src0_sel:DWORD src1_sel:BYTE_2
	v_lshlrev_b32_sdwa v249, s32, v2 dst_sel:DWORD dst_unused:UNUSED_PAD src0_sel:DWORD src1_sel:BYTE_3
	s_waitcnt vmcnt(2) lgkmcnt(0)
	s_barrier
	s_andn2_b64 vcc, exec, s[42:43]
	s_cbranch_vccnz .LBB0_1279
	s_waitcnt lgkmcnt(0)
	ds_read_b128 v[86:89], v85 offset:49248
	ds_read_b128 v[90:93], v85 offset:49216
	ds_read_b128 v[94:97], v85 offset:49184
	ds_read_b128 v[98:101], v85 offset:49152
	s_waitcnt lgkmcnt(3)
	v_pk_mul_f32 v[32:33], v[32:33], v[86:87]
	s_waitcnt lgkmcnt(2)
	v_pk_mul_f32 v[28:29], v[28:29], v[90:91]
	s_waitcnt lgkmcnt(1)
	v_pk_mul_f32 v[24:25], v[24:25], v[94:95]
	v_pk_mul_f32 v[34:35], v[34:35], v[88:89]
	v_pk_mul_f32 v[30:31], v[30:31], v[92:93]
	v_pk_mul_f32 v[26:27], v[26:27], v[96:97]
	s_waitcnt lgkmcnt(0)
	v_pk_mul_f32 v[22:23], v[22:23], v[100:101]
	v_pk_mul_f32 v[20:21], v[20:21], v[98:99]
	v_pk_mul_f32 v[16:17], v[16:17], v[86:87]
	v_pk_mul_f32 v[12:13], v[12:13], v[90:91]
	v_pk_mul_f32 v[8:9], v[8:9], v[94:95]
	v_pk_mul_f32 v[18:19], v[18:19], v[88:89]
	v_pk_mul_f32 v[14:15], v[14:15], v[92:93]
	v_pk_mul_f32 v[10:11], v[10:11], v[96:97]
	v_pk_mul_f32 v[6:7], v[6:7], v[100:101]
	v_pk_mul_f32 v[4:5], v[4:5], v[98:99]
	v_pk_mul_f32 v[240:241], v[240:241], v[86:87]
	v_pk_mul_f32 v[236:237], v[236:237], v[90:91]
	v_pk_mul_f32 v[232:233], v[232:233], v[94:95]
	v_pk_mul_f32 v[242:243], v[242:243], v[88:89]
	v_pk_mul_f32 v[238:239], v[238:239], v[92:93]
	v_pk_mul_f32 v[234:235], v[234:235], v[96:97]
	v_pk_mul_f32 v[230:231], v[230:231], v[100:101]
	v_pk_mul_f32 v[228:229], v[228:229], v[98:99]

;   #define RESC() do{ if(resc){ asm volatile("s_waitcnt lgkmcnt(0)":::"memory"); \
;       _Pragma("unroll") for(int d_=0;d_<2;++d_) _Pragma("unroll") for(int r=0;r<16;++r)o[d_][r]*=wsf[crow(r,hi)]; } }while(0)
;   #define ROT() do{sl_prev=sl_cur;sl_cur=sl_next;sl_next=(sl_next==(NSLOT-1)*SLOTB)?0:sl_next+SLOTB;}while(0)
;   #define ENDW(tt) do{ if((tt)+3<NT){WAIT_BAR(2);} else if((tt)+2<NT){WAIT_BAR(1);} else {WAIT_BAR(0);} }while(0)
; template<int THRL> __device__ __forceinline__ void attn_unit(int b,int h,int qb,const bf16*Q,const bf16*__restrict__ K,const bf16*__restrict__ V,bf16*O,const unsigned*MASK,char*shm){
;     ...
;   for(;t+1<NT;t+=2){
;     STEP(pB0,pB1,pA0,pA1,t,(t+3<NT),(t+1<NT),(t+1<NT),wB,wA);       ENDW(t);   RESC(); ROT();
;     STEP(pA0,pA1,pB0,pB1,t+1,(t+4<NT),(t+2<NT),(t+2<NT),wA,wB);     ENDW(t+1); RESC(); ROT();
.LBB0_1290:
	global_load_dword v223, v[210:211], off
	v_add_u32_e32 v85, s48, v220
	ds_read_b64_tr_b16 v[186:187], v85 offset:24576
	ds_read_b64_tr_b16 v[188:189], v85 offset:25088
	s_waitcnt lgkmcnt(9)
	v_mfma_f32_32x32x16_bf16 v[102:117], v[178:181], v[138:141], v[36:51]
	v_cvt_pk_bf16_f32 v146, v68, v69
	v_cvt_pk_bf16_f32 v147, v70, v71
	ds_read_b64_tr_b16 v[178:179], v85 offset:28672
	ds_read_b64_tr_b16 v[180:181], v85 offset:29184
	s_waitcnt lgkmcnt(10)
	v_mfma_f32_32x32x16_bf16 v[86:101], v[170:173], v[138:141], v[36:51]
	v_cvt_pk_bf16_f32 v148, v72, v73
	v_cvt_pk_bf16_f32 v149, v74, v75
	ds_read_b64_tr_b16 v[182:183], v85 offset:25600
	ds_read_b64_tr_b16 v[184:185], v85 offset:26112
	s_waitcnt lgkmcnt(11)
	v_mfma_f32_32x32x16_bf16 v[102:117], v[174:177], v[134:137], v[102:117]
	v_cvt_pk_bf16_f32 v142, v76, v77
	v_cvt_pk_bf16_f32 v143, v78, v79
	ds_read_b64_tr_b16 v[76:77], v85 offset:29696
	ds_read_b64_tr_b16 v[78:79], v85 offset:30208
	s_waitcnt lgkmcnt(12)
	v_mfma_f32_32x32x16_bf16 v[86:101], v[162:165], v[134:137], v[86:101]
	v_cvt_pk_bf16_f32 v144, v80, v81
	v_cvt_pk_bf16_f32 v145, v82, v83
	ds_read_b64_tr_b16 v[72:73], v85 offset:26624
	ds_read_b64_tr_b16 v[74:75], v85 offset:27136
	s_waitcnt lgkmcnt(13)
	v_mfma_f32_32x32x16_bf16 v[102:117], v[166:169], v[126:129], v[102:117]
	v_cvt_pk_bf16_f32 v130, v52, v53
	v_cvt_pk_bf16_f32 v131, v54, v55
	ds_read_b64_tr_b16 v[68:69], v85 offset:30720
	ds_read_b64_tr_b16 v[70:71], v85 offset:31232
	s_waitcnt lgkmcnt(14)
	v_mfma_f32_32x32x16_bf16 v[86:101], v[154:157], v[126:129], v[86:101]
	v_cvt_pk_bf16_f32 v132, v56, v57
	v_cvt_pk_bf16_f32 v133, v58, v59
	ds_read_b64_tr_b16 v[56:57], v85 offset:27648
	ds_read_b64_tr_b16 v[58:59], v85 offset:28160
	s_waitcnt lgkmcnt(14)
	v_mfma_f32_32x32x16_bf16 v[102:117], v[158:161], v[122:125], v[102:117]
	v_cvt_pk_bf16_f32 v118, v60, v61
	v_cvt_pk_bf16_f32 v119, v62, v63
	ds_read_b64_tr_b16 v[52:53], v85 offset:31744
	ds_read_b64_tr_b16 v[54:55], v85 offset:32256
	v_mfma_f32_32x32x16_bf16 v[86:101], v[150:153], v[122:125], v[86:101]
	v_cvt_pk_bf16_f32 v120, v64, v65
	v_cvt_pk_bf16_f32 v121, v66, v67
	ds_read_b128 v[80:83], v225 offset:51200
	s_add_i32 s65, s64, -1
	s_cmp_ge_i32 s65, s61
	s_cselect_b64 s[48:49], -1, 0
	s_and_b64 vcc, exec, s[48:49]
	s_cbranch_vccnz .LBB0_1292
	v_lshl_add_u64 v[62:63], v[194:195], 0, s[46:47]
	s_add_i32 s4, s60, s58
	v_lshl_add_u64 v[62:63], v[62:63], 0, s[82:83]
	s_mov_b32 s5, m0
	s_mov_b32 m0, s4
	s_nop 0
	global_load_lds_dwordx4 v[62:63], off
	s_mov_b32 m0, s5

.LBB0_1293:
	s_waitcnt lgkmcnt(0)
	v_and_b32_e32 v146, v146, v80
	v_and_b32_e32 v147, v147, v81
	v_and_b32_e32 v148, v148, v82
	v_and_b32_e32 v149, v149, v83
	ds_read_b128 v[80:83], v226 offset:51200
	s_waitcnt lgkmcnt(14)
	v_mfma_f32_32x32x16_bf16 v[20:35], v[146:149], v[186:189], v[20:35]
	v_exp_f32_e32 v102, v102
	v_exp_f32_e32 v103, v103
	v_exp_f32_e32 v104, v104
	v_exp_f32_e32 v105, v105
	s_waitcnt lgkmcnt(12)
	v_mfma_f32_32x32x16_bf16 v[4:19], v[146:149], v[178:181], v[4:19]
	v_mfma_f32_32x32x16_bf16 v[228:243], v[146:149], v[204:207], v[228:243]
	v_exp_f32_e32 v106, v106
	v_exp_f32_e32 v107, v107
	v_exp_f32_e32 v108, v108
	v_exp_f32_e32 v109, v109
	s_waitcnt lgkmcnt(0)
	v_and_b32_e32 v142, v142, v80
	v_and_b32_e32 v143, v143, v81
	v_and_b32_e32 v144, v144, v82
	v_and_b32_e32 v145, v145, v83
	ds_read_b128 v[80:83], v248 offset:51200
	v_add_u32_e32 v60, s62, v221
	ds_read_b128 v[178:181], v60
	ds_read_b128 v[170:173], v60 offset:512
	s_waitcnt lgkmcnt(12)
	v_mfma_f32_32x32x16_bf16 v[20:35], v[142:145], v[182:185], v[20:35]
	v_exp_f32_e32 v110, v110
	v_exp_f32_e32 v111, v111
	v_exp_f32_e32 v112, v112
	v_exp_f32_e32 v113, v113
	ds_read_b128 v[174:177], v60 offset:2048
	ds_read_b128 v[162:165], v60 offset:2560
	s_waitcnt lgkmcnt(12)
	v_mfma_f32_32x32x16_bf16 v[4:19], v[142:145], v[76:79], v[4:19]
	v_mfma_f32_32x32x16_bf16 v[228:243], v[142:145], v[204:207], v[228:243]
	v_exp_f32_e32 v114, v114
	v_exp_f32_e32 v115, v115
	v_exp_f32_e32 v116, v116
	v_exp_f32_e32 v117, v117
	s_waitcnt lgkmcnt(4)
	v_and_b32_e32 v130, v130, v80
	v_and_b32_e32 v131, v131, v81
	v_and_b32_e32 v132, v132, v82
	v_and_b32_e32 v133, v133, v83
	ds_read_b128 v[80:83], v249 offset:51200
	ds_read_b128 v[166:169], v60 offset:4096
	ds_read_b128 v[154:157], v60 offset:4608
	s_waitcnt lgkmcnt(12)
	v_mfma_f32_32x32x16_bf16 v[20:35], v[130:133], v[72:75], v[20:35]
	v_exp_f32_e32 v86, v86
	v_exp_f32_e32 v87, v87
	v_exp_f32_e32 v88, v88
	v_exp_f32_e32 v89, v89
	ds_read_b128 v[158:161], v60 offset:6144
	ds_read_b128 v[150:153], v60 offset:6656
	s_waitcnt lgkmcnt(12)
	v_mfma_f32_32x32x16_bf16 v[4:19], v[130:133], v[68:71], v[4:19]
	v_mfma_f32_32x32x16_bf16 v[228:243], v[130:133], v[204:207], v[228:243]
	v_exp_f32_e32 v90, v90
	v_exp_f32_e32 v91, v91
	v_exp_f32_e32 v92, v92
	v_exp_f32_e32 v93, v93
	s_waitcnt lgkmcnt(4)
	v_and_b32_e32 v118, v118, v80
	v_and_b32_e32 v119, v119, v81
	v_and_b32_e32 v120, v120, v82
	v_and_b32_e32 v121, v121, v83
	s_nop 0
	s_waitcnt lgkmcnt(10)
	v_mfma_f32_32x32x16_bf16 v[20:35], v[118:121], v[56:59], v[20:35]
	v_exp_f32_e32 v94, v94
	v_exp_f32_e32 v95, v95
	v_exp_f32_e32 v96, v96
	v_exp_f32_e32 v97, v97
	s_waitcnt lgkmcnt(8)
	v_mfma_f32_32x32x16_bf16 v[4:19], v[118:121], v[52:55], v[4:19]
	v_mfma_f32_32x32x16_bf16 v[228:243], v[118:121], v[204:207], v[228:243]
	v_exp_f32_e32 v98, v98
	v_exp_f32_e32 v99, v99
	v_exp_f32_e32 v100, v100
	v_exp_f32_e32 v101, v101
	v_lshlrev_b32_sdwa v225, s32, v218 dst_sel:DWORD dst_unused:UNUSED_PAD src0_sel:DWORD src1_sel:BYTE_0
	v_lshlrev_b32_sdwa v226, s32, v218 dst_sel:DWORD dst_unused:UNUSED_PAD src0_sel:DWORD src1_sel:BYTE_1
	v_lshlrev_b32_sdwa v248, s32, v218 dst_sel:DWORD dst_unused:UNUSED_PAD src0_sel:DWORD src1_sel:BYTE_2
	v_lshlrev_b32_sdwa v249, s32, v218 dst_sel:DWORD dst_unused:UNUSED_PAD src0_sel:DWORD src1_sel:BYTE_3
	s_mov_b64 s[4:5], -1
	s_and_b64 vcc, exec, s[48:49]
	s_cbranch_vccnz .LBB0_1318
	s_andn2_b64 vcc, exec, s[4:5]
	s_cbranch_vccz .LBB0_1323

.LBB0_1299:
	v_add_u32_e32 v255, s60, v220
	ds_read_b64_tr_b16 v[190:191], v255 offset:24576
	ds_read_b64_tr_b16 v[192:193], v255 offset:25088
	s_waitcnt lgkmcnt(9)
	v_mfma_f32_32x32x16_bf16 v[68:83], v[178:181], v[138:141], v[36:51]
	v_cvt_pk_bf16_f32 v146, v102, v103
	v_cvt_pk_bf16_f32 v147, v104, v105
	ds_read_b64_tr_b16 v[186:187], v255 offset:28672
	ds_read_b64_tr_b16 v[188:189], v255 offset:29184
	s_waitcnt lgkmcnt(10)
	v_mfma_f32_32x32x16_bf16 v[52:67], v[170:173], v[138:141], v[36:51]
	v_cvt_pk_bf16_f32 v148, v106, v107
	v_cvt_pk_bf16_f32 v149, v108, v109
	ds_read_b64_tr_b16 v[182:183], v255 offset:25600
	ds_read_b64_tr_b16 v[184:185], v255 offset:26112
	s_waitcnt lgkmcnt(11)
	v_mfma_f32_32x32x16_bf16 v[68:83], v[174:177], v[134:137], v[68:83]
	v_cvt_pk_bf16_f32 v142, v110, v111
	v_cvt_pk_bf16_f32 v143, v112, v113
	ds_read_b64_tr_b16 v[110:111], v255 offset:29696
	ds_read_b64_tr_b16 v[112:113], v255 offset:30208
	s_waitcnt lgkmcnt(12)
	v_mfma_f32_32x32x16_bf16 v[52:67], v[162:165], v[134:137], v[52:67]
	v_cvt_pk_bf16_f32 v144, v114, v115
	v_cvt_pk_bf16_f32 v145, v116, v117
	ds_read_b64_tr_b16 v[106:107], v255 offset:26624
	ds_read_b64_tr_b16 v[108:109], v255 offset:27136
	s_waitcnt lgkmcnt(13)
	v_mfma_f32_32x32x16_bf16 v[68:83], v[166:169], v[126:129], v[68:83]
	v_cvt_pk_bf16_f32 v130, v86, v87
	v_cvt_pk_bf16_f32 v131, v88, v89
	ds_read_b64_tr_b16 v[102:103], v255 offset:30720
	ds_read_b64_tr_b16 v[104:105], v255 offset:31232
	s_waitcnt lgkmcnt(14)
	v_mfma_f32_32x32x16_bf16 v[52:67], v[154:157], v[126:129], v[52:67]
	v_cvt_pk_bf16_f32 v132, v90, v91
	v_cvt_pk_bf16_f32 v133, v92, v93
	ds_read_b64_tr_b16 v[90:91], v255 offset:27648
	ds_read_b64_tr_b16 v[92:93], v255 offset:28160
	s_waitcnt lgkmcnt(14)
	v_mfma_f32_32x32x16_bf16 v[68:83], v[158:161], v[122:125], v[68:83]
	v_cvt_pk_bf16_f32 v118, v94, v95
	v_cvt_pk_bf16_f32 v119, v96, v97
	ds_read_b64_tr_b16 v[86:87], v255 offset:31744
	ds_read_b64_tr_b16 v[88:89], v255 offset:32256
	v_mfma_f32_32x32x16_bf16 v[52:67], v[150:153], v[122:125], v[52:67]
	v_cvt_pk_bf16_f32 v120, v98, v99
	v_cvt_pk_bf16_f32 v121, v100, v101
	ds_read_b128 v[114:117], v225 offset:51200
	s_cmp_ge_i32 s64, s61
	s_cselect_b64 s[50:51], -1, 0
	s_and_b64 vcc, exec, s[50:51]
	s_cbranch_vccnz .LBB0_1301
	v_lshl_add_u64 v[96:97], v[194:195], 0, s[46:47]
	s_mov_b64 s[4:5], 0x40000
	s_add_i32 s42, s62, s58
	v_lshl_add_u64 v[96:97], v[96:97], 0, s[4:5]
	s_mov_b32 s4, m0
	s_mov_b32 m0, s42
	s_nop 0
	global_load_lds_dwordx4 v[96:97], off
	s_mov_b32 m0, s4

.LBB0_1310:
	s_waitcnt lgkmcnt(6)
	v_mfma_f32_32x32x16_bf16 v[20:35], v[130:133], v[106:109], v[20:35]
	v_exp_f32_e32 v52, v52
	v_exp_f32_e32 v53, v53
	v_exp_f32_e32 v54, v54
	v_exp_f32_e32 v55, v55
	s_and_b64 vcc, exec, s[42:43]
	s_cbranch_vccnz .LBB0_1312
	v_add_u32_e32 v85, s60, v221
	ds_read_b128 v[158:161], v85 offset:6144
	ds_read_b128 v[150:153], v85 offset:6656
.LBB0_1312:
	s_waitcnt lgkmcnt(4)
	v_mfma_f32_32x32x16_bf16 v[4:19], v[130:133], v[102:105], v[4:19]
	v_mfma_f32_32x32x16_bf16 v[228:243], v[130:133], v[204:207], v[228:243]
	v_exp_f32_e32 v56, v56
	v_exp_f32_e32 v57, v57
	v_exp_f32_e32 v58, v58
	v_exp_f32_e32 v59, v59
	s_waitcnt lgkmcnt(0)
	v_and_b32_e32 v118, v118, v114
	v_and_b32_e32 v119, v119, v115
	v_and_b32_e32 v120, v120, v116
	v_and_b32_e32 v121, v121, v117
	s_nop 0
	s_waitcnt lgkmcnt(2)
	v_mfma_f32_32x32x16_bf16 v[20:35], v[118:121], v[90:93], v[20:35]
	v_exp_f32_e32 v60, v60
	v_exp_f32_e32 v61, v61
	v_exp_f32_e32 v62, v62
	v_exp_f32_e32 v63, v63
	s_waitcnt lgkmcnt(0)
	v_mfma_f32_32x32x16_bf16 v[4:19], v[118:121], v[86:89], v[4:19]
	v_mfma_f32_32x32x16_bf16 v[228:243], v[118:121], v[204:207], v[228:243]
	v_exp_f32_e32 v64, v64
	v_exp_f32_e32 v65, v65
	v_exp_f32_e32 v66, v66
	v_exp_f32_e32 v67, v67
	v_lshlrev_b32_sdwa v225, s32, v223 dst_sel:DWORD dst_unused:UNUSED_PAD src0_sel:DWORD src1_sel:BYTE_0
	v_lshlrev_b32_sdwa v226, s32, v223 dst_sel:DWORD dst_unused:UNUSED_PAD src0_sel:DWORD src1_sel:BYTE_1
	v_lshlrev_b32_sdwa v248, s32, v223 dst_sel:DWORD dst_unused:UNUSED_PAD src0_sel:DWORD src1_sel:BYTE_2
	v_lshlrev_b32_sdwa v249, s32, v223 dst_sel:DWORD dst_unused:UNUSED_PAD src0_sel:DWORD src1_sel:BYTE_3
	s_mov_b64 s[4:5], -1
	s_and_b64 vcc, exec, s[50:51]
	s_cbranch_vccnz .LBB0_1324
	s_andn2_b64 vcc, exec, s[4:5]
	s_cbranch_vccz .LBB0_1329

.LBB0_1337:
	v_add_u32_e32 v2, s62, v220
	ds_read_b64_tr_b16 v[114:115], v2 offset:24576
	ds_read_b64_tr_b16 v[116:117], v2 offset:25088
	s_waitcnt lgkmcnt(9)
	v_mfma_f32_32x32x16_bf16 v[86:101], v[178:181], v[138:141], v[36:51]
	v_cvt_pk_bf16_f32 v146, v68, v69
	v_cvt_pk_bf16_f32 v147, v70, v71
	ds_read_b64_tr_b16 v[110:111], v2 offset:28672
	ds_read_b64_tr_b16 v[112:113], v2 offset:29184
	s_waitcnt lgkmcnt(10)
	v_mfma_f32_32x32x16_bf16 v[36:51], v[170:173], v[138:141], v[36:51]
	v_cvt_pk_bf16_f32 v148, v72, v73
	v_cvt_pk_bf16_f32 v149, v74, v75
	ds_read_b64_tr_b16 v[106:107], v2 offset:25600
	ds_read_b64_tr_b16 v[108:109], v2 offset:26112
	s_waitcnt lgkmcnt(11)
	v_mfma_f32_32x32x16_bf16 v[86:101], v[174:177], v[134:137], v[86:101]
	v_cvt_pk_bf16_f32 v142, v76, v77
	v_cvt_pk_bf16_f32 v143, v78, v79
	ds_read_b64_tr_b16 v[102:103], v2 offset:29696
	ds_read_b64_tr_b16 v[104:105], v2 offset:30208
	s_waitcnt lgkmcnt(12)
	v_mfma_f32_32x32x16_bf16 v[36:51], v[162:165], v[134:137], v[36:51]
	v_cvt_pk_bf16_f32 v144, v80, v81
	v_cvt_pk_bf16_f32 v145, v82, v83
	ds_read_b64_tr_b16 v[80:81], v2 offset:26624
	ds_read_b64_tr_b16 v[82:83], v2 offset:27136
	s_waitcnt lgkmcnt(13)
	v_mfma_f32_32x32x16_bf16 v[86:101], v[166:169], v[126:129], v[86:101]
	v_cvt_pk_bf16_f32 v130, v52, v53
	v_cvt_pk_bf16_f32 v131, v54, v55
	ds_read_b64_tr_b16 v[76:77], v2 offset:30720
	ds_read_b64_tr_b16 v[78:79], v2 offset:31232
	s_waitcnt lgkmcnt(14)
	v_mfma_f32_32x32x16_bf16 v[36:51], v[154:157], v[126:129], v[36:51]
	v_cvt_pk_bf16_f32 v132, v56, v57
	v_cvt_pk_bf16_f32 v133, v58, v59
	ds_read_b64_tr_b16 v[72:73], v2 offset:27648
	ds_read_b64_tr_b16 v[74:75], v2 offset:28160
	s_waitcnt lgkmcnt(14)
	v_mfma_f32_32x32x16_bf16 v[86:101], v[158:161], v[122:125], v[86:101]
	v_cvt_pk_bf16_f32 v118, v60, v61
	v_cvt_pk_bf16_f32 v119, v62, v63
	ds_read_b64_tr_b16 v[68:69], v2 offset:31744
	ds_read_b64_tr_b16 v[70:71], v2 offset:32256
	v_mfma_f32_32x32x16_bf16 v[36:51], v[150:153], v[122:125], v[36:51]
	v_cvt_pk_bf16_f32 v120, v64, v65
	v_cvt_pk_bf16_f32 v121, v66, v67
	ds_read_b128 v[154:157], v225 offset:51200
	v_max_f32_e32 v52, v87, v87
	v_max_f32_e32 v53, v86, v86
	v_max_f32_e32 v52, v53, v52
	s_nop 3
	v_max3_f32 v53, v88, v89, v37
	v_max3_f32 v52, v52, v36, v38
	v_max3_f32 v52, v52, v39, v90
	v_max3_f32 v53, v53, v92, v93
	v_max3_f32 v52, v52, v91, v40
	v_max3_f32 v53, v53, v42, v43
	v_max3_f32 v52, v52, v41, v94
	v_max3_f32 v53, v53, v96, v97
	v_max3_f32 v52, v52, v95, v44
	v_max3_f32 v53, v53, v46, v47
	v_max3_f32 v52, v52, v45, v98
	v_max3_f32 v53, v53, v100, v101
	v_max3_f32 v52, v52, v99, v48
	v_max3_f32 v53, v53, v50, v51
	v_max3_f32 v52, v52, v49, v53
	v_mov_b32_e32 v53, v52
	s_nop 1
	v_permlane32_swap_b32_e32 v52, v53
	v_max_f32_e32 v53, v53, v53
	v_max_f32_e32 v52, v52, v52
	v_max_f32_e32 v52, v52, v53
	v_cmp_lt_f32_e32 vcc, s14, v52
	s_cmp_lg_u64 vcc, 0
	s_cselect_b64 s[40:41], -1, 0
	s_cbranch_vccnz .LBB0_1342
.LBB0_1338:
	s_waitcnt lgkmcnt(0)
	v_and_b32_e32 v146, v146, v154
	v_and_b32_e32 v147, v147, v155
	v_and_b32_e32 v148, v148, v156
	v_and_b32_e32 v149, v149, v157
	ds_read_b128 v[154:157], v226 offset:51200
	s_waitcnt lgkmcnt(14)
	v_mfma_f32_32x32x16_bf16 v[20:35], v[146:149], v[114:117], v[20:35]
	v_exp_f32_e32 v86, v86
	v_exp_f32_e32 v87, v87
	v_exp_f32_e32 v88, v88
	v_exp_f32_e32 v89, v89
	s_waitcnt lgkmcnt(12)
	v_mfma_f32_32x32x16_bf16 v[4:19], v[146:149], v[110:113], v[4:19]
	v_mfma_f32_32x32x16_bf16 v[228:243], v[146:149], v[204:207], v[228:243]
	v_exp_f32_e32 v90, v90
	v_exp_f32_e32 v91, v91
	v_exp_f32_e32 v92, v92
	v_exp_f32_e32 v93, v93
	s_waitcnt lgkmcnt(0)
	v_and_b32_e32 v142, v142, v154
	v_and_b32_e32 v143, v143, v155
	v_and_b32_e32 v144, v144, v156
	v_and_b32_e32 v145, v145, v157
	ds_read_b128 v[154:157], v248 offset:51200
	s_waitcnt lgkmcnt(10)
	v_mfma_f32_32x32x16_bf16 v[20:35], v[142:145], v[106:109], v[20:35]
	v_exp_f32_e32 v94, v94
	v_exp_f32_e32 v95, v95
	v_exp_f32_e32 v96, v96
	v_exp_f32_e32 v97, v97
	s_waitcnt lgkmcnt(8)
	v_mfma_f32_32x32x16_bf16 v[4:19], v[142:145], v[102:105], v[4:19]
	v_mfma_f32_32x32x16_bf16 v[228:243], v[142:145], v[204:207], v[228:243]
	v_exp_f32_e32 v98, v98
	v_exp_f32_e32 v99, v99
	v_exp_f32_e32 v100, v100
	v_exp_f32_e32 v101, v101
	s_waitcnt lgkmcnt(0)
	v_and_b32_e32 v130, v130, v154
	v_and_b32_e32 v131, v131, v155
	v_and_b32_e32 v132, v132, v156
	v_and_b32_e32 v133, v133, v157
	ds_read_b128 v[154:157], v249 offset:51200
	s_waitcnt lgkmcnt(6)
	v_mfma_f32_32x32x16_bf16 v[20:35], v[130:133], v[80:83], v[20:35]
	v_exp_f32_e32 v36, v36
	v_exp_f32_e32 v37, v37
	v_exp_f32_e32 v38, v38
	v_exp_f32_e32 v39, v39
	s_waitcnt lgkmcnt(4)
	v_mfma_f32_32x32x16_bf16 v[4:19], v[130:133], v[76:79], v[4:19]
	v_mfma_f32_32x32x16_bf16 v[228:243], v[130:133], v[204:207], v[228:243]
	v_exp_f32_e32 v40, v40
	v_exp_f32_e32 v41, v41
	v_exp_f32_e32 v42, v42
	v_exp_f32_e32 v43, v43
	s_waitcnt lgkmcnt(0)
	v_and_b32_e32 v118, v118, v154
	v_and_b32_e32 v119, v119, v155
	v_and_b32_e32 v120, v120, v156
	v_and_b32_e32 v121, v121, v157
	s_nop 0
	s_waitcnt lgkmcnt(2)
	v_mfma_f32_32x32x16_bf16 v[20:35], v[118:121], v[72:75], v[20:35]
	v_exp_f32_e32 v44, v44
	v_exp_f32_e32 v45, v45
	v_exp_f32_e32 v46, v46
	v_exp_f32_e32 v47, v47
	s_waitcnt lgkmcnt(0)
	v_mfma_f32_32x32x16_bf16 v[4:19], v[118:121], v[68:71], v[4:19]
	v_mfma_f32_32x32x16_bf16 v[228:243], v[118:121], v[204:207], v[228:243]
	v_exp_f32_e32 v48, v48
	v_exp_f32_e32 v49, v49
	v_exp_f32_e32 v50, v50
	v_exp_f32_e32 v51, v51
	v_lshlrev_b32_sdwa v225, s32, v218 dst_sel:DWORD dst_unused:UNUSED_PAD src0_sel:DWORD src1_sel:BYTE_0
	v_lshlrev_b32_sdwa v226, s32, v218 dst_sel:DWORD dst_unused:UNUSED_PAD src0_sel:DWORD src1_sel:BYTE_1
	v_lshlrev_b32_sdwa v248, s32, v218 dst_sel:DWORD dst_unused:UNUSED_PAD src0_sel:DWORD src1_sel:BYTE_2
	v_lshlrev_b32_sdwa v249, s32, v218 dst_sel:DWORD dst_unused:UNUSED_PAD src0_sel:DWORD src1_sel:BYTE_3
	s_andn2_b64 vcc, exec, s[40:41]
	v_lshl_add_u32 v52, v214, 4, s57
	s_cbranch_vccnz .LBB0_1340
; #define SBAR() __builtin_amdgcn_sched_barrier(0)
;   #define RESC() do{ if(resc){ asm volatile("s_waitcnt lgkmcnt(0)":::"memory"); \
;       _Pragma("unroll") for(int d_=0;d_<2;++d_) _Pragma("unroll") for(int r=0;r<16;++r)o[d_][r]*=wsf[crow(r,hi)]; } }while(0)
;   #define PKW(P,B) cvtpk_s(P[B],P[B+1])
; __device__ __forceinline__ void pv(f32x16*o,int vb,bf16x8 pa0,bf16x8 pa1,bf16x8 pa2,bf16x8 pa3){
;   #pragma unroll
;   for(int d0=0;d0<2;++d0){s16x4 lo[4],hi[4];
;     #pragma unroll
;     for(int ks=0;ks<4;++ks){
;       asm volatile("ds_read_b64_tr_b16 %0,%1 offset:%c2":"=&v"(lo[ks]):"v"(vb),"i"(d0*4096+ks*1024):"memory");
;       asm volatile("ds_read_b64_tr_b16 %0,%1 offset:%c2":"=&v"(hi[ks]):"v"(vb),"i"(d0*4096+ks*1024+512):"memory");}
;     asm volatile("s_waitcnt lgkmcnt(0)":::"memory");SBAR();
;     ...
;     o[d0]=__builtin_amdgcn_mfma_f32_32x32x16_bf16(pa0,PK(0),o[d0],0,0,0);
;     o[d0]=__builtin_amdgcn_mfma_f32_32x32x16_bf16(pa1,PK(1),o[d0],0,0,0);
;     o[d0]=__builtin_amdgcn_mfma_f32_32x32x16_bf16(pa2,PK(2),o[d0],0,0,0);
;     o[d0]=__builtin_amdgcn_mfma_f32_32x32x16_bf16(pa3,PK(3),o[d0],0,0,0);
;     ...
;   }
; }
; template<int THRL> __device__ __forceinline__ void attn_unit(int b,int h,int qb,const bf16*Q,const bf16*__restrict__ K,const bf16*__restrict__ V,bf16*O,const unsigned*MASK,char*shm){
;     ...
;   STEP(pB0,pB1,pA0,pA1,NT-1,false,false,false,wB,wA); RESC();
;   { float sacc=pB0[0]+pB0[1]; _Pragma("unroll") for(int r=2;r<16;++r)sacc+=pB0[r]; _Pragma("unroll") for(int r=0;r<16;++r)sacc+=pB1[r]; l_reg+=sacc;
;     pw0=(u32x4){PKW(pB0,0),PKW(pB0,2),PKW(pB0,4),PKW(pB0,6)};pw1=(u32x4){PKW(pB0,8),PKW(pB0,10),PKW(pB0,12),PKW(pB0,14)};pw2=(u32x4){PKW(pB1,0),PKW(pB1,2),PKW(pB1,4),PKW(pB1,6)};pw3=(u32x4){PKW(pB1,8),PKW(pB1,10),PKW(pB1,12),PKW(pB1,14)};
;     SBAR(); pv(o,vb0+sl_cur,PAF(0),PAF(1),PAF(2),PAF(3)); }
;     ...
;   {auto rr=__builtin_amdgcn_permlane32_swap(__float_as_uint(l_reg),__float_as_uint(l_reg),false,false);l_reg=__uint_as_float(rr[0])+__uint_as_float(rr[1]);}
;   if(hi==0)wsf[32+r32]=l_reg;asm volatile("s_waitcnt lgkmcnt(0)":::"memory");
	s_waitcnt lgkmcnt(0)
	ds_read_b128 v[54:57], v52 offset:49248
	ds_read_b128 v[58:61], v52 offset:49216
	ds_read_b128 v[62:65], v52 offset:49184
	ds_read_b128 v[66:69], v52 offset:49152
	s_waitcnt lgkmcnt(3)
	v_pk_mul_f32 v[34:35], v[34:35], v[56:57]
	s_waitcnt lgkmcnt(2)
	v_pk_mul_f32 v[30:31], v[30:31], v[60:61]
	s_waitcnt lgkmcnt(1)
	v_pk_mul_f32 v[26:27], v[26:27], v[64:65]
	s_waitcnt lgkmcnt(0)
	v_pk_mul_f32 v[22:23], v[22:23], v[68:69]
	v_pk_mul_f32 v[32:33], v[32:33], v[54:55]
	v_pk_mul_f32 v[28:29], v[28:29], v[58:59]
	v_pk_mul_f32 v[24:25], v[24:25], v[62:63]
	v_pk_mul_f32 v[20:21], v[20:21], v[66:67]
	v_pk_mul_f32 v[18:19], v[18:19], v[56:57]
	v_pk_mul_f32 v[14:15], v[14:15], v[60:61]
	v_pk_mul_f32 v[10:11], v[10:11], v[64:65]
	v_pk_mul_f32 v[6:7], v[6:7], v[68:69]
	v_pk_mul_f32 v[16:17], v[16:17], v[54:55]
	v_pk_mul_f32 v[12:13], v[12:13], v[58:59]
	v_pk_mul_f32 v[8:9], v[8:9], v[62:63]
	v_pk_mul_f32 v[4:5], v[4:5], v[66:67]
	v_pk_mul_f32 v[242:243], v[242:243], v[56:57]
	v_pk_mul_f32 v[238:239], v[238:239], v[60:61]
	v_pk_mul_f32 v[234:235], v[234:235], v[64:65]
	v_pk_mul_f32 v[230:231], v[230:231], v[68:69]
	v_pk_mul_f32 v[240:241], v[240:241], v[54:55]
	v_pk_mul_f32 v[236:237], v[236:237], v[58:59]
	v_pk_mul_f32 v[232:233], v[232:233], v[62:63]
	v_pk_mul_f32 v[228:229], v[228:229], v[66:67]
.LBB0_1340:
	s_cmp_lg_u32 0, -1
	s_cselect_b32 s4, 0, 0
	s_addk_i32 s4, 0x6000
	v_cvt_pk_bf16_f32 v36, v36, v37
	v_add3_u32 v53, v217, s4, v215
	v_cvt_pk_bf16_f32 v54, v86, v87
	v_cvt_pk_bf16_f32 v55, v88, v89
	v_cvt_pk_bf16_f32 v56, v90, v91
	v_cvt_pk_bf16_f32 v57, v92, v93
	v_cvt_pk_bf16_f32 v58, v94, v95
	v_cvt_pk_bf16_f32 v59, v96, v97
	v_cvt_pk_bf16_f32 v60, v98, v99
	v_cvt_pk_bf16_f32 v61, v100, v101
	v_cvt_pk_bf16_f32 v37, v38, v39
	v_cvt_pk_bf16_f32 v38, v40, v41
	v_cvt_pk_bf16_f32 v39, v42, v43
	v_cvt_pk_bf16_f32 v40, v44, v45
	v_cvt_pk_bf16_f32 v41, v46, v47
	v_cvt_pk_bf16_f32 v42, v48, v49
	v_cvt_pk_bf16_f32 v43, v50, v51
	ds_read_b128 v[86:89], v225 offset:51200
	ds_read_b128 v[90:93], v226 offset:51200
	ds_read_b128 v[94:97], v248 offset:51200
	ds_read_b128 v[98:101], v249 offset:51200
	v_add3_u32 v53, v53, v216, s60
	ds_read_b64_tr_b16 v[44:45],v53 offset:0
	ds_read_b64_tr_b16 v[46:47],v53 offset:512
	ds_read_b64_tr_b16 v[48:49],v53 offset:1024
	ds_read_b64_tr_b16 v[50:51],v53 offset:1536
	ds_read_b64_tr_b16 v[62:63],v53 offset:2048
	ds_read_b64_tr_b16 v[64:65],v53 offset:2560
	ds_read_b64_tr_b16 v[66:67],v53 offset:3072
	ds_read_b64_tr_b16 v[68:69],v53 offset:3584
	s_waitcnt lgkmcnt(0)
	v_and_b32_e32 v54, v54, v86
	v_and_b32_e32 v55, v55, v87
	v_and_b32_e32 v56, v56, v88
	v_and_b32_e32 v57, v57, v89
	v_and_b32_e32 v58, v58, v90
	v_and_b32_e32 v59, v59, v91
	v_and_b32_e32 v60, v60, v92
	v_and_b32_e32 v61, v61, v93
	v_and_b32_e32 v36, v36, v94
	v_and_b32_e32 v37, v37, v95
	v_and_b32_e32 v38, v38, v96
	v_and_b32_e32 v39, v39, v97
	v_and_b32_e32 v40, v40, v98
	v_and_b32_e32 v41, v41, v99
	v_and_b32_e32 v42, v42, v100
	v_and_b32_e32 v43, v43, v101
	s_nop 0
	v_mfma_f32_32x32x16_bf16 v[20:35], v[54:57], v[44:47], v[20:35]
	ds_read_b64_tr_b16 v[44:45],v53 offset:4096
	ds_read_b64_tr_b16 v[46:47],v53 offset:4608
	v_mfma_f32_32x32x16_bf16 v[20:35], v[58:61], v[48:51], v[20:35]
	ds_read_b64_tr_b16 v[48:49],v53 offset:5120
	ds_read_b64_tr_b16 v[50:51],v53 offset:5632
	v_mfma_f32_32x32x16_bf16 v[20:35], v[36:39], v[62:65], v[20:35]
	ds_read_b64_tr_b16 v[62:63],v53 offset:6144
	ds_read_b64_tr_b16 v[64:65],v53 offset:6656
	v_mfma_f32_32x32x16_bf16 v[20:35], v[40:43], v[66:69], v[20:35]
	v_mfma_f32_32x32x16_bf16 v[228:243], v[54:57], v[204:207], v[228:243]
	v_mfma_f32_32x32x16_bf16 v[228:243], v[58:61], v[204:207], v[228:243]
	v_mfma_f32_32x32x16_bf16 v[228:243], v[36:39], v[204:207], v[228:243]
	v_mfma_f32_32x32x16_bf16 v[228:243], v[40:43], v[204:207], v[228:243]
	ds_read_b64_tr_b16 v[66:67],v53 offset:7168
	ds_read_b64_tr_b16 v[68:69],v53 offset:7680
	s_waitcnt lgkmcnt(0)
	v_mfma_f32_32x32x16_bf16 v[4:19], v[54:57], v[44:47], v[4:19]
	v_cmp_gt_u32_e32 vcc, 32, v1
	v_mfma_f32_32x32x16_bf16 v[4:19], v[58:61], v[48:51], v[4:19]
	v_mfma_f32_32x32x16_bf16 v[4:19], v[36:39], v[62:65], v[4:19]
	v_mov_b32_e32 v36, v2
	s_nop 1
	v_permlane32_swap_b32_e32 v2, v36
	v_mfma_f32_32x32x16_bf16 v[4:19], v[40:43], v[66:69], v[4:19]
	s_and_saveexec_b64 s[4:5], vcc
	s_cbranch_execz .LBB0_1260
	v_lshl_add_u32 v37, v213, 2, s57
	v_add_f32_e32 v2, v2, v36
	ds_write_b32 v37, v2 offset:49280
	s_branch .LBB0_1260
